# v56 + attention tile loops: row-sum chain split into two independent f32 accumulators (v254/v255) to remove the dependent-add latency chain
# speedup vs baseline: 1.0121x; 1.0121x over previous
.LBB0_953:
	v_add_u32_e32 v168, s34, v240
	ds_read_b64_tr_b16 v[164:165], v168 offset:24576
	ds_read_b64_tr_b16 v[166:167], v168 offset:25088
	v_add_f32_e32 v254, v52, v53
	v_add_f32_e32 v255, v54, v55
	v_add_f32_e32 v254, v56, v254
	v_add_f32_e32 v255, v57, v255
	s_waitcnt lgkmcnt(9)
	v_mfma_f32_32x32x16_bf16 v[68:83], v[160:163], v[116:119], 0
	v_cvt_pk_bf16_f32 v128, v52, v53
	v_cvt_pk_bf16_f32 v129, v54, v55
	ds_read_b64_tr_b16 v[160:161], v168 offset:28672
	ds_read_b64_tr_b16 v[162:163], v168 offset:29184
	v_add_f32_e32 v254, v58, v254
	v_add_f32_e32 v255, v59, v255
	v_add_f32_e32 v254, v60, v254
	v_add_f32_e32 v255, v61, v255
	v_cvt_pk_bf16_f32 v130, v56, v57
	v_cvt_pk_bf16_f32 v131, v58, v59
	s_waitcnt lgkmcnt(10)
	v_mfma_f32_32x32x16_bf16 v[84:99], v[152:155], v[116:119], 0
	ds_read_b64_tr_b16 v[152:153], v168 offset:25600
	ds_read_b64_tr_b16 v[154:155], v168 offset:26112
	s_waitcnt lgkmcnt(11)
	v_mfma_f32_32x32x16_bf16 v[68:83], v[156:159], v[108:111], v[68:83]
	v_add_f32_e32 v254, v62, v254
	v_add_f32_e32 v255, v63, v255
	v_add_f32_e32 v254, v64, v254
	v_add_f32_e32 v255, v65, v255
	v_cvt_pk_bf16_f32 v124, v60, v61
	v_cvt_pk_bf16_f32 v125, v62, v63
	ds_read_b64_tr_b16 v[156:157], v168 offset:29696
	ds_read_b64_tr_b16 v[158:159], v168 offset:30208
	v_add_f32_e32 v254, v66, v254
	v_add_f32_e32 v255, v67, v255
	v_add_f32_e32 v254, v36, v254
	v_add_f32_e32 v255, v37, v255
	v_cvt_pk_bf16_f32 v126, v64, v65
	v_cvt_pk_bf16_f32 v127, v66, v67
	s_waitcnt lgkmcnt(12)
	v_mfma_f32_32x32x16_bf16 v[84:99], v[148:151], v[108:111], v[84:99]
	ds_read_b64_tr_b16 v[148:149], v168 offset:26624
	ds_read_b64_tr_b16 v[150:151], v168 offset:27136
	s_waitcnt lgkmcnt(13)
	v_mfma_f32_32x32x16_bf16 v[68:83], v[144:147], v[104:107], v[68:83]
	v_add_f32_e32 v254, v38, v254
	v_add_f32_e32 v255, v39, v255
	v_add_f32_e32 v254, v40, v254
	v_add_f32_e32 v255, v41, v255
	v_cvt_pk_bf16_f32 v120, v36, v37
	v_cvt_pk_bf16_f32 v121, v38, v39
	ds_read_b64_tr_b16 v[144:145], v168 offset:30720
	ds_read_b64_tr_b16 v[146:147], v168 offset:31232
	v_add_f32_e32 v254, v42, v254
	v_add_f32_e32 v255, v43, v255
	v_add_f32_e32 v254, v44, v254
	v_add_f32_e32 v255, v45, v255
	v_cvt_pk_bf16_f32 v122, v40, v41
	v_cvt_pk_bf16_f32 v123, v42, v43
	s_waitcnt lgkmcnt(14)
	v_mfma_f32_32x32x16_bf16 v[84:99], v[140:143], v[104:107], v[84:99]
	ds_read_b64_tr_b16 v[140:141], v168 offset:27648
	ds_read_b64_tr_b16 v[142:143], v168 offset:28160
	s_waitcnt lgkmcnt(14)
	v_mfma_f32_32x32x16_bf16 v[68:83], v[136:139], v[100:103], v[68:83]
	v_add_f32_e32 v254, v46, v254
	v_add_f32_e32 v255, v47, v255
	v_add_f32_e32 v254, v48, v254
	v_add_f32_e32 v255, v49, v255
	v_cvt_pk_bf16_f32 v112, v44, v45
	v_cvt_pk_bf16_f32 v113, v46, v47
	ds_read_b64_tr_b16 v[136:137], v168 offset:31744
	ds_read_b64_tr_b16 v[138:139], v168 offset:32256
	v_add_f32_e32 v254, v50, v254
	v_add_f32_e32 v255, v51, v255
	v_add_f32_e32 v36, v254, v255
	v_mfma_f32_32x32x16_bf16 v[84:99], v[132:135], v[100:103], v[84:99]
	v_add_f32_e32 v133, 0, v36
	v_cvt_pk_bf16_f32 v114, v48, v49
	v_cvt_pk_bf16_f32 v115, v50, v51
	v_lshl_add_u64 v[184:185], v[182:183], 0, s[18:19]
	s_mov_b64 s[34:35], 0x13080000
	v_lshl_add_u64 v[36:37], v[184:185], 0, s[34:35]
	s_add_i32 s34, s67, s58
	s_mov_b32 s35, m0
	s_mov_b32 m0, s34
	s_nop 0
	global_load_lds_dwordx4 v[36:37], off
	s_mov_b32 m0, s35
	v_lshl_add_u64 v[186:187], v[180:181], 0, s[18:19]
	s_mov_b64 s[34:35], 0x15040000
	v_lshl_add_u64 v[36:37], v[186:187], 0, s[34:35]
	s_add_i32 s34, s7, s59
	s_mov_b32 s35, m0
	s_mov_b32 m0, s34
	s_nop 0
	global_load_lds_dwordx4 v[36:37], off
	s_mov_b32 m0, s35
	ds_read_b128 v[36:39], v191
	ds_read_b128 v[40:43], v191 offset:32
	ds_read_b128 v[44:47], v191 offset:128
	v_sub_f32_e32 v132, v237, v239
	v_add_f32_e32 v192, v241, v133
	s_waitcnt lgkmcnt(2)
	v_pk_add_f32 v[36:37], v[132:133], v[36:37] op_sel_hi:[0,1] neg_lo:[0,1] neg_hi:[0,1]
	v_pk_add_f32 v[38:39], v[132:133], v[38:39] op_sel_hi:[0,1] neg_lo:[0,1] neg_hi:[0,1]
	v_pk_add_f32 v[52:53], v[68:69], v[36:37]
	s_waitcnt lgkmcnt(0)
	v_pk_add_f32 v[36:37], v[132:133], v[44:45] op_sel_hi:[0,1] neg_lo:[0,1] neg_hi:[0,1]
	v_pk_add_f32 v[54:55], v[70:71], v[38:39]
	v_pk_add_f32 v[38:39], v[132:133], v[46:47] op_sel_hi:[0,1] neg_lo:[0,1] neg_hi:[0,1]
	ds_read_b128 v[44:47], v191 offset:160
	v_pk_add_f32 v[40:41], v[132:133], v[40:41] op_sel_hi:[0,1] neg_lo:[0,1] neg_hi:[0,1]
	v_pk_add_f32 v[42:43], v[132:133], v[42:43] op_sel_hi:[0,1] neg_lo:[0,1] neg_hi:[0,1]
	v_pk_add_f32 v[56:57], v[72:73], v[40:41]
	v_pk_add_f32 v[58:59], v[74:75], v[42:43]
	s_waitcnt lgkmcnt(0)
	v_pk_add_f32 v[40:41], v[132:133], v[44:45] op_sel_hi:[0,1] neg_lo:[0,1] neg_hi:[0,1]
	v_pk_add_f32 v[42:43], v[132:133], v[46:47] op_sel_hi:[0,1] neg_lo:[0,1] neg_hi:[0,1]
	ds_read_b128 v[44:47], v191 offset:64
	ds_read_b128 v[48:51], v191 offset:192
	v_pk_add_f32 v[36:37], v[84:85], v[36:37]
	v_pk_add_f32 v[38:39], v[86:87], v[38:39]
	v_pk_add_f32 v[40:41], v[88:89], v[40:41]
	s_waitcnt lgkmcnt(1)
	v_pk_add_f32 v[44:45], v[132:133], v[44:45] op_sel_hi:[0,1] neg_lo:[0,1] neg_hi:[0,1]
	v_pk_add_f32 v[46:47], v[132:133], v[46:47] op_sel_hi:[0,1] neg_lo:[0,1] neg_hi:[0,1]
	v_pk_add_f32 v[60:61], v[76:77], v[44:45]
	s_waitcnt lgkmcnt(0)
	v_pk_add_f32 v[44:45], v[132:133], v[48:49] op_sel_hi:[0,1] neg_lo:[0,1] neg_hi:[0,1]
	v_pk_add_f32 v[62:63], v[78:79], v[46:47]
	v_pk_add_f32 v[46:47], v[132:133], v[50:51] op_sel_hi:[0,1] neg_lo:[0,1] neg_hi:[0,1]
	ds_read_b128 v[48:51], v191 offset:96
	ds_read_b128 v[66:69], v191 offset:224
	v_pk_add_f32 v[42:43], v[90:91], v[42:43]
	v_pk_add_f32 v[44:45], v[92:93], v[44:45]
	v_pk_add_f32 v[46:47], v[94:95], v[46:47]
	s_waitcnt lgkmcnt(1)
	v_pk_add_f32 v[48:49], v[132:133], v[48:49] op_sel_hi:[0,1] neg_lo:[0,1] neg_hi:[0,1]
	v_pk_add_f32 v[50:51], v[132:133], v[50:51] op_sel_hi:[0,1] neg_lo:[0,1] neg_hi:[0,1]
	v_pk_add_f32 v[64:65], v[80:81], v[48:49]
	s_waitcnt lgkmcnt(0)
	v_pk_add_f32 v[48:49], v[132:133], v[66:67] op_sel_hi:[0,1] neg_lo:[0,1] neg_hi:[0,1]
	v_pk_add_f32 v[66:67], v[82:83], v[50:51]
	v_pk_add_f32 v[50:51], v[132:133], v[68:69] op_sel_hi:[0,1] neg_lo:[0,1] neg_hi:[0,1]
	v_max_f32_e32 v68, v52, v53
	v_max3_f32 v69, v54, v55, v37
	v_max3_f32 v68, v68, v36, v38
	v_max3_f32 v68, v68, v39, v56
	v_max3_f32 v69, v69, v58, v59
	v_max3_f32 v68, v68, v57, v40
	v_max3_f32 v69, v69, v42, v43
	v_max3_f32 v68, v68, v41, v60
	v_max3_f32 v69, v69, v62, v63
	v_max3_f32 v68, v68, v61, v44
	v_max3_f32 v69, v69, v46, v47
	v_pk_add_f32 v[48:49], v[96:97], v[48:49]
	v_pk_add_f32 v[50:51], v[98:99], v[50:51]
	v_max3_f32 v68, v68, v45, v64
	v_max3_f32 v69, v69, v66, v67
	v_max3_f32 v68, v68, v65, v48
	v_max3_f32 v69, v69, v50, v51
	v_max3_f32 v68, v68, v49, v69
	v_mov_b32_e32 v69, v68
	s_nop 1
	v_permlane32_swap_b32_e32 v68, v69
	v_max_f32_e32 v69, v69, v69
	v_max_f32_e32 v68, v68, v68
	v_max_f32_e32 v68, v68, v69
	v_cmp_lt_f32_e32 vcc, s94, v68
	s_cmp_lg_u64 vcc, 0
	s_cselect_b64 s[34:35], -1, 0
	s_cbranch_vccnz .LBB0_961

.LBB0_956:
	s_add_i32 s34, s7, 0x2000
	s_cmpk_lg_i32 s7, 0x4000
	s_cselect_b32 s61, s34, 0
	v_add_u32_e32 v174, s67, v240
	ds_read_b64_tr_b16 v[144:145], v174 offset:24576
	ds_read_b64_tr_b16 v[146:147], v174 offset:25088
	v_add_f32_e32 v254, v52, v53
	v_add_f32_e32 v255, v54, v55
	v_add_f32_e32 v254, v56, v254
	v_add_f32_e32 v255, v57, v255
	s_waitcnt lgkmcnt(9)
	v_mfma_f32_32x32x16_bf16 v[68:83], v[68:71], v[116:119], 0
	v_cvt_pk_bf16_f32 v128, v52, v53
	v_cvt_pk_bf16_f32 v129, v54, v55
	ds_read_b64_tr_b16 v[140:141], v174 offset:28672
	ds_read_b64_tr_b16 v[142:143], v174 offset:29184
	v_add_f32_e32 v254, v58, v254
	v_add_f32_e32 v255, v59, v255
	v_add_f32_e32 v254, v60, v254
	v_add_f32_e32 v255, v61, v255
	v_cvt_pk_bf16_f32 v130, v56, v57
	v_cvt_pk_bf16_f32 v131, v58, v59
	s_waitcnt lgkmcnt(10)
	v_mfma_f32_32x32x16_bf16 v[84:99], v[84:87], v[116:119], 0
	ds_read_b64_tr_b16 v[132:133], v174 offset:25600
	ds_read_b64_tr_b16 v[134:135], v174 offset:26112
	s_waitcnt lgkmcnt(11)
	v_mfma_f32_32x32x16_bf16 v[68:83], v[168:171], v[108:111], v[68:83]
	v_add_f32_e32 v254, v62, v254
	v_add_f32_e32 v255, v63, v255
	v_add_f32_e32 v254, v64, v254
	v_add_f32_e32 v255, v65, v255
	v_cvt_pk_bf16_f32 v124, v60, v61
	v_cvt_pk_bf16_f32 v125, v62, v63
	ds_read_b64_tr_b16 v[136:137], v174 offset:29696
	ds_read_b64_tr_b16 v[138:139], v174 offset:30208
	v_add_f32_e32 v254, v66, v254
	v_add_f32_e32 v255, v67, v255
	v_add_f32_e32 v254, v36, v254
	v_add_f32_e32 v255, v37, v255
	v_cvt_pk_bf16_f32 v126, v64, v65
	v_cvt_pk_bf16_f32 v127, v66, v67
	s_waitcnt lgkmcnt(12)
	v_mfma_f32_32x32x16_bf16 v[84:99], v[164:167], v[108:111], v[84:99]
	ds_read_b64_tr_b16 v[176:177], v174 offset:26624
	ds_read_b64_tr_b16 v[178:179], v174 offset:27136
	s_waitcnt lgkmcnt(13)
	v_mfma_f32_32x32x16_bf16 v[68:83], v[160:163], v[104:107], v[68:83]
	v_add_f32_e32 v254, v38, v254
	v_add_f32_e32 v255, v39, v255
	v_add_f32_e32 v254, v40, v254
	v_add_f32_e32 v255, v41, v255
	v_cvt_pk_bf16_f32 v120, v36, v37
	v_cvt_pk_bf16_f32 v121, v38, v39
	ds_read_b64_tr_b16 v[164:165], v174 offset:30720
	ds_read_b64_tr_b16 v[166:167], v174 offset:31232
	v_add_f32_e32 v254, v42, v254
	v_add_f32_e32 v255, v43, v255
	v_add_f32_e32 v254, v44, v254
	v_add_f32_e32 v255, v45, v255
	v_cvt_pk_bf16_f32 v122, v40, v41
	v_cvt_pk_bf16_f32 v123, v42, v43
	s_waitcnt lgkmcnt(14)
	v_mfma_f32_32x32x16_bf16 v[84:99], v[152:155], v[104:107], v[84:99]
	ds_read_b64_tr_b16 v[168:169], v174 offset:27648
	ds_read_b64_tr_b16 v[170:171], v174 offset:28160
	s_waitcnt lgkmcnt(14)
	v_mfma_f32_32x32x16_bf16 v[68:83], v[156:159], v[100:103], v[68:83]
	v_add_f32_e32 v254, v46, v254
	v_add_f32_e32 v255, v47, v255
	v_add_f32_e32 v254, v48, v254
	v_add_f32_e32 v255, v49, v255
	v_cvt_pk_bf16_f32 v112, v44, v45
	v_cvt_pk_bf16_f32 v113, v46, v47
	ds_read_b64_tr_b16 v[172:173], v174 offset:31744
	ds_read_b64_tr_b16 v[174:175], v174 offset:32256
	v_add_f32_e32 v254, v50, v254
	v_add_f32_e32 v255, v51, v255
	v_add_f32_e32 v36, v254, v255
	v_mfma_f32_32x32x16_bf16 v[84:99], v[148:151], v[100:103], v[84:99]
	v_add_f32_e32 v149, 0, v36
	v_cvt_pk_bf16_f32 v114, v48, v49
	v_cvt_pk_bf16_f32 v115, v50, v51
	s_mov_b64 s[34:35], 0x130a0000
	v_lshl_add_u64 v[36:37], v[184:185], 0, s[34:35]
	s_add_i32 s34, s7, s58
	s_mov_b32 s35, m0
	s_mov_b32 m0, s34
	s_nop 0
	global_load_lds_dwordx4 v[36:37], off
	s_mov_b32 m0, s35
	s_mov_b64 s[34:35], 0x15060000
	v_lshl_add_u64 v[36:37], v[186:187], 0, s[34:35]
	s_add_i32 s34, s61, s59
	s_mov_b32 s35, m0
	s_mov_b32 m0, s34
	s_nop 0
	global_load_lds_dwordx4 v[36:37], off
	s_mov_b32 m0, s35
	ds_read_b128 v[36:39], v191 offset:256
	ds_read_b128 v[40:43], v191 offset:288
	ds_read_b128 v[44:47], v191 offset:384
	v_sub_f32_e32 v148, v237, v239
	v_add_f32_e32 v241, v192, v149
	s_waitcnt lgkmcnt(2)
	v_pk_add_f32 v[36:37], v[148:149], v[36:37] op_sel_hi:[0,1] neg_lo:[0,1] neg_hi:[0,1]
	v_pk_add_f32 v[38:39], v[148:149], v[38:39] op_sel_hi:[0,1] neg_lo:[0,1] neg_hi:[0,1]
	v_pk_add_f32 v[52:53], v[68:69], v[36:37]
	s_waitcnt lgkmcnt(0)
	v_pk_add_f32 v[36:37], v[148:149], v[44:45] op_sel_hi:[0,1] neg_lo:[0,1] neg_hi:[0,1]
	v_pk_add_f32 v[54:55], v[70:71], v[38:39]
	v_pk_add_f32 v[38:39], v[148:149], v[46:47] op_sel_hi:[0,1] neg_lo:[0,1] neg_hi:[0,1]
	ds_read_b128 v[44:47], v191 offset:416
	v_pk_add_f32 v[40:41], v[148:149], v[40:41] op_sel_hi:[0,1] neg_lo:[0,1] neg_hi:[0,1]
	v_pk_add_f32 v[42:43], v[148:149], v[42:43] op_sel_hi:[0,1] neg_lo:[0,1] neg_hi:[0,1]
	v_pk_add_f32 v[56:57], v[72:73], v[40:41]
	v_pk_add_f32 v[58:59], v[74:75], v[42:43]
	s_waitcnt lgkmcnt(0)
	v_pk_add_f32 v[40:41], v[148:149], v[44:45] op_sel_hi:[0,1] neg_lo:[0,1] neg_hi:[0,1]
	v_pk_add_f32 v[42:43], v[148:149], v[46:47] op_sel_hi:[0,1] neg_lo:[0,1] neg_hi:[0,1]
	ds_read_b128 v[44:47], v191 offset:320
	ds_read_b128 v[48:51], v191 offset:448
	v_pk_add_f32 v[36:37], v[84:85], v[36:37]
	v_pk_add_f32 v[38:39], v[86:87], v[38:39]
	v_pk_add_f32 v[40:41], v[88:89], v[40:41]
	s_waitcnt lgkmcnt(1)
	v_pk_add_f32 v[44:45], v[148:149], v[44:45] op_sel_hi:[0,1] neg_lo:[0,1] neg_hi:[0,1]
	v_pk_add_f32 v[46:47], v[148:149], v[46:47] op_sel_hi:[0,1] neg_lo:[0,1] neg_hi:[0,1]
	v_pk_add_f32 v[60:61], v[76:77], v[44:45]
	s_waitcnt lgkmcnt(0)
	v_pk_add_f32 v[44:45], v[148:149], v[48:49] op_sel_hi:[0,1] neg_lo:[0,1] neg_hi:[0,1]
	v_pk_add_f32 v[62:63], v[78:79], v[46:47]
	v_pk_add_f32 v[46:47], v[148:149], v[50:51] op_sel_hi:[0,1] neg_lo:[0,1] neg_hi:[0,1]
	ds_read_b128 v[48:51], v191 offset:352
	ds_read_b128 v[66:69], v191 offset:480
	v_pk_add_f32 v[42:43], v[90:91], v[42:43]
	v_pk_add_f32 v[44:45], v[92:93], v[44:45]
	v_pk_add_f32 v[46:47], v[94:95], v[46:47]
	s_waitcnt lgkmcnt(1)
	v_pk_add_f32 v[48:49], v[148:149], v[48:49] op_sel_hi:[0,1] neg_lo:[0,1] neg_hi:[0,1]
	v_pk_add_f32 v[50:51], v[148:149], v[50:51] op_sel_hi:[0,1] neg_lo:[0,1] neg_hi:[0,1]
	v_pk_add_f32 v[64:65], v[80:81], v[48:49]
	s_waitcnt lgkmcnt(0)
	v_pk_add_f32 v[48:49], v[148:149], v[66:67] op_sel_hi:[0,1] neg_lo:[0,1] neg_hi:[0,1]
	v_pk_add_f32 v[66:67], v[82:83], v[50:51]
	v_pk_add_f32 v[50:51], v[148:149], v[68:69] op_sel_hi:[0,1] neg_lo:[0,1] neg_hi:[0,1]
	v_max_f32_e32 v68, v52, v53
	v_max3_f32 v69, v54, v55, v37
	v_max3_f32 v68, v68, v36, v38
	v_max3_f32 v68, v68, v39, v56
	v_max3_f32 v69, v69, v58, v59
	v_max3_f32 v68, v68, v57, v40
	v_max3_f32 v69, v69, v42, v43
	v_max3_f32 v68, v68, v41, v60
	v_max3_f32 v69, v69, v62, v63
	v_max3_f32 v68, v68, v61, v44
	v_max3_f32 v69, v69, v46, v47
	v_pk_add_f32 v[48:49], v[96:97], v[48:49]
	v_pk_add_f32 v[50:51], v[98:99], v[50:51]
	v_max3_f32 v68, v68, v45, v64
	v_max3_f32 v69, v69, v66, v67
	v_max3_f32 v68, v68, v65, v48
	v_max3_f32 v69, v69, v50, v51
	v_max3_f32 v68, v68, v49, v69
	v_mov_b32_e32 v69, v68
	s_nop 1
	v_permlane32_swap_b32_e32 v68, v69
	v_max_f32_e32 v69, v69, v69
	v_max_f32_e32 v68, v68, v68
	v_max_f32_e32 v68, v68, v69
	v_cmp_lt_f32_e32 vcc, s94, v68
	s_cmp_lg_u64 vcc, 0
	s_cselect_b64 s[34:35], -1, 0
	s_cbranch_vccnz .LBB0_964

.LBB0_969:
	s_mov_b64 s[64:65], 0x80
	v_add_u32_e32 v2, s38, v240
	ds_read_b64_tr_b16 v[164:165], v2 offset:24576
	ds_read_b64_tr_b16 v[166:167], v2 offset:25088
	v_add_f32_e32 v254, v52, v53
	v_add_f32_e32 v255, v54, v55
	v_add_f32_e32 v254, v56, v254
	v_add_f32_e32 v255, v57, v255
	v_cvt_pk_bf16_f32 v128, v52, v53
	v_cvt_pk_bf16_f32 v129, v54, v55
	s_waitcnt lgkmcnt(3)
	v_mfma_f32_32x32x16_bf16 v[84:99], v[160:163], v[116:119], 0
	ds_read_b64_tr_b16 v[160:161], v2 offset:28672
	ds_read_b64_tr_b16 v[162:163], v2 offset:29184
	v_add_f32_e32 v254, v58, v254
	s_waitcnt lgkmcnt(4)
	v_mfma_f32_32x32x16_bf16 v[68:83], v[152:155], v[116:119], 0
	v_add_f32_e32 v255, v59, v255
	v_add_f32_e32 v254, v60, v254
	v_add_f32_e32 v255, v61, v255
	v_cvt_pk_bf16_f32 v130, v56, v57
	v_cvt_pk_bf16_f32 v131, v58, v59
	ds_read_b64_tr_b16 v[116:117], v2 offset:25600
	ds_read_b64_tr_b16 v[118:119], v2 offset:26112
	v_add_f32_e32 v254, v62, v254
	v_add_f32_e32 v255, v63, v255
	v_add_f32_e32 v254, v64, v254
	v_add_f32_e32 v255, v65, v255
	v_cvt_pk_bf16_f32 v124, v60, v61
	v_cvt_pk_bf16_f32 v125, v62, v63
	v_mfma_f32_32x32x16_bf16 v[84:99], v[156:159], v[108:111], v[84:99]
	ds_read_b64_tr_b16 v[152:153], v2 offset:29696
	ds_read_b64_tr_b16 v[154:155], v2 offset:30208
	v_mfma_f32_32x32x16_bf16 v[68:83], v[148:151], v[108:111], v[68:83]
	v_add_f32_e32 v254, v66, v254
	v_add_f32_e32 v255, v67, v255
	v_add_f32_e32 v254, v36, v254
	v_add_f32_e32 v255, v37, v255
	v_cvt_pk_bf16_f32 v126, v64, v65
	v_cvt_pk_bf16_f32 v127, v66, v67
	ds_read_b64_tr_b16 v[108:109], v2 offset:26624
	ds_read_b64_tr_b16 v[110:111], v2 offset:27136
	v_add_f32_e32 v254, v38, v254
	v_add_f32_e32 v255, v39, v255
	v_add_f32_e32 v254, v40, v254
	v_add_f32_e32 v255, v41, v255
	v_cvt_pk_bf16_f32 v120, v36, v37
	v_cvt_pk_bf16_f32 v121, v38, v39
	v_mfma_f32_32x32x16_bf16 v[84:99], v[144:147], v[104:107], v[84:99]
	ds_read_b64_tr_b16 v[144:145], v2 offset:30720
	ds_read_b64_tr_b16 v[146:147], v2 offset:31232
	v_mfma_f32_32x32x16_bf16 v[68:83], v[140:143], v[104:107], v[68:83]
	v_add_f32_e32 v254, v42, v254
	v_add_f32_e32 v255, v43, v255
	v_add_f32_e32 v254, v44, v254
	v_add_f32_e32 v255, v45, v255
	v_cvt_pk_bf16_f32 v122, v40, v41
	v_cvt_pk_bf16_f32 v123, v42, v43
	ds_read_b64_tr_b16 v[104:105], v2 offset:27648
	ds_read_b64_tr_b16 v[106:107], v2 offset:28160
	v_add_f32_e32 v254, v46, v254
	v_add_f32_e32 v255, v47, v255
	v_add_f32_e32 v254, v48, v254
	v_add_f32_e32 v255, v49, v255
	v_cvt_pk_bf16_f32 v112, v44, v45
	v_cvt_pk_bf16_f32 v113, v46, v47
	v_mfma_f32_32x32x16_bf16 v[84:99], v[136:139], v[100:103], v[84:99]
	ds_read_b64_tr_b16 v[136:137], v2 offset:31744
	ds_read_b64_tr_b16 v[138:139], v2 offset:32256
	v_mfma_f32_32x32x16_bf16 v[68:83], v[132:135], v[100:103], v[68:83]
	v_add_f32_e32 v254, v50, v254
	v_add_f32_e32 v255, v51, v255
	v_add_f32_e32 v2, v254, v255
	v_add_f32_e32 v2, 0, v2
	v_cvt_pk_bf16_f32 v114, v48, v49
	v_cvt_pk_bf16_f32 v115, v50, v51
	v_lshl_add_u32 v64, v235, 2, s57
	ds_read_b128 v[36:39], v64 offset:768
	ds_read_b128 v[40:43], v64 offset:800
	ds_read_b128 v[44:47], v64 offset:896
	ds_read_b128 v[48:51], v64 offset:928
	ds_read_b128 v[52:55], v64 offset:832
	ds_read_b128 v[56:59], v64 offset:864
	ds_read_b128 v[60:63], v64 offset:960
	ds_read_b128 v[64:67], v64 offset:992
	v_sub_f32_e32 v100, v237, v239
	s_waitcnt lgkmcnt(7)
	v_sub_f32_e32 v37, v100, v37
	v_sub_f32_e32 v36, v100, v36
	s_waitcnt lgkmcnt(3)
	v_sub_f32_e32 v53, v100, v53
	v_sub_f32_e32 v52, v100, v52
	v_sub_f32_e32 v39, v100, v39
	v_sub_f32_e32 v38, v100, v38
	v_pk_add_f32 v[38:39], v[86:87], v[38:39]
	v_pk_add_f32 v[86:87], v[92:93], v[52:53]
	v_pk_add_f32 v[52:53], v[84:85], v[36:37]
	v_sub_f32_e32 v37, v100, v45
	v_sub_f32_e32 v36, v100, v44
	s_waitcnt lgkmcnt(0)
; __device__ __forceinline__ void cmask(f32x16&p0,f32x16&p1,int jb,int qrel,int hi){
;   const float NEG=-INFINITY; int kb=64*jb+4*hi;
;   #pragma unroll
;   for(int r=0;r<16;++r){int kv=kb+(r&3)+8*(r>>2); if(kv>qrel)p0[r]=NEG; if(kv+32>qrel)p1[r]=NEG;}
; }
	v_sub_f32_e32 v45, v100, v67
	v_sub_f32_e32 v44, v100, v66
	v_sub_f32_e32 v47, v100, v47
	v_sub_f32_e32 v46, v100, v46
	v_pk_add_f32 v[46:47], v[70:71], v[46:47]
	v_pk_add_f32 v[70:71], v[82:83], v[44:45]
	v_or_b32_e32 v45, 0xe0, v235
	v_pk_add_f32 v[36:37], v[68:69], v[36:37]
	v_or_b32_e32 v44, 0xc0, v235
	v_cmp_le_i32_e32 vcc, v45, v236
	v_sub_f32_e32 v55, v100, v55
	v_sub_f32_e32 v54, v100, v54
	v_cndmask_b32_e32 v36, v222, v36, vcc
	v_cmp_lt_i32_e32 vcc, v44, v236
	v_sub_f32_e32 v41, v100, v41
	v_sub_f32_e32 v40, v100, v40
	v_cndmask_b32_e32 v53, v222, v53, vcc
	v_cmp_le_i32_e32 vcc, v44, v236
	v_or_b32_e32 v44, 0xe1, v235
	v_pk_add_f32 v[40:41], v[88:89], v[40:41]
	v_cndmask_b32_e32 v52, v222, v52, vcc
	v_cmp_le_i32_e32 vcc, v44, v236
	v_or_b32_e32 v44, 0xc2, v235
	v_pk_add_f32 v[88:89], v[94:95], v[54:55]
	v_sub_f32_e32 v55, v100, v65
	v_sub_f32_e32 v54, v100, v64
	v_cndmask_b32_e32 v37, v222, v37, vcc
	v_cmp_le_i32_e32 vcc, v44, v236
	v_pk_add_f32 v[66:67], v[80:81], v[54:55]
	v_or_b32_e32 v44, 0xc3, v235
	v_cndmask_b32_e32 v54, v222, v38, vcc
	v_or_b32_e32 v38, 0xe2, v235
	v_cmp_le_i32_e32 vcc, v38, v236
	v_sub_f32_e32 v57, v100, v57
	v_sub_f32_e32 v56, v100, v56
	v_cndmask_b32_e32 v38, v222, v46, vcc
	v_cmp_le_i32_e32 vcc, v44, v236
	v_sub_f32_e32 v43, v100, v43
	v_sub_f32_e32 v42, v100, v42
	v_cndmask_b32_e32 v55, v222, v39, vcc
	v_or_b32_e32 v39, 0xe3, v235
	v_cmp_le_i32_e32 vcc, v39, v236
	v_or_b32_e32 v44, 0xc8, v235
	v_pk_add_f32 v[42:43], v[90:91], v[42:43]
	v_pk_add_f32 v[90:91], v[96:97], v[56:57]
	v_sub_f32_e32 v57, v100, v63
	v_sub_f32_e32 v56, v100, v62
	v_cndmask_b32_e32 v39, v222, v47, vcc
	v_cmp_le_i32_e32 vcc, v44, v236
	v_sub_f32_e32 v49, v100, v49
	v_sub_f32_e32 v48, v100, v48
	v_pk_add_f32 v[64:65], v[78:79], v[56:57]
	v_cndmask_b32_e32 v56, v222, v40, vcc
	v_or_b32_e32 v40, 0xe8, v235
	v_pk_add_f32 v[48:49], v[72:73], v[48:49]
	v_cmp_le_i32_e32 vcc, v40, v236
	v_or_b32_e32 v44, 0xc9, v235
	v_sub_f32_e32 v59, v100, v59
	v_cndmask_b32_e32 v40, v222, v48, vcc
	v_cmp_le_i32_e32 vcc, v44, v236
	v_sub_f32_e32 v58, v100, v58
	v_or_b32_e32 v44, 0xca, v235
	v_cndmask_b32_e32 v57, v222, v41, vcc
	v_or_b32_e32 v41, 0xe9, v235
	v_cmp_le_i32_e32 vcc, v41, v236
	v_pk_add_f32 v[92:93], v[98:99], v[58:59]
	v_sub_f32_e32 v59, v100, v61
	v_sub_f32_e32 v58, v100, v60
	v_cndmask_b32_e32 v41, v222, v49, vcc
	v_cmp_le_i32_e32 vcc, v44, v236
	v_sub_f32_e32 v51, v100, v51
	v_sub_f32_e32 v50, v100, v50
	v_pk_add_f32 v[62:63], v[76:77], v[58:59]
	v_cndmask_b32_e32 v58, v222, v42, vcc
	v_or_b32_e32 v42, 0xea, v235
	v_pk_add_f32 v[50:51], v[74:75], v[50:51]
	v_cmp_le_i32_e32 vcc, v42, v236
	v_or_b32_e32 v44, 0xcb, v235
	v_or_b32_e32 v45, 0xd1, v235
	v_cndmask_b32_e32 v42, v222, v50, vcc
	v_cmp_le_i32_e32 vcc, v44, v236
	v_or_b32_e32 v44, 0xd0, v235
	v_or_b32_e32 v46, 0xd2, v235
	v_cndmask_b32_e32 v59, v222, v43, vcc
	v_or_b32_e32 v43, 0xeb, v235
	v_cmp_le_i32_e32 vcc, v43, v236
	v_or_b32_e32 v47, 0xd3, v235
	v_or_b32_e32 v48, 0xd8, v235
	v_cndmask_b32_e32 v43, v222, v51, vcc
	v_cmp_le_i32_e32 vcc, v44, v236
	v_or_b32_e32 v44, 0xf0, v235
	v_or_b32_e32 v49, 0xd9, v235
	v_cndmask_b32_e32 v60, v222, v86, vcc
	v_cmp_le_i32_e32 vcc, v44, v236
	v_max_f32_e32 v68, v52, v53
	v_or_b32_e32 v50, 0xda, v235
	v_cndmask_b32_e32 v44, v222, v62, vcc
	v_cmp_le_i32_e32 vcc, v45, v236
	v_or_b32_e32 v45, 0xf1, v235
	v_max3_f32 v69, v54, v55, v37
	v_cndmask_b32_e32 v61, v222, v87, vcc
	v_cmp_le_i32_e32 vcc, v45, v236
	v_max3_f32 v68, v68, v36, v38
	v_max3_f32 v68, v68, v39, v56
	v_cndmask_b32_e32 v45, v222, v63, vcc
	v_cmp_le_i32_e32 vcc, v46, v236
	v_or_b32_e32 v46, 0xf2, v235
	v_max3_f32 v69, v69, v58, v59
	v_cndmask_b32_e32 v62, v222, v88, vcc
	v_cmp_le_i32_e32 vcc, v46, v236
	v_or_b32_e32 v51, 0xdb, v235
	v_max3_f32 v68, v68, v57, v40
	v_cndmask_b32_e32 v46, v222, v64, vcc
	v_cmp_le_i32_e32 vcc, v47, v236
	v_or_b32_e32 v47, 0xf3, v235
	v_max3_f32 v69, v69, v42, v43
	v_cndmask_b32_e32 v63, v222, v89, vcc
	v_cmp_le_i32_e32 vcc, v47, v236
	v_max3_f32 v68, v68, v41, v60
	v_max3_f32 v69, v69, v62, v63
	v_cndmask_b32_e32 v47, v222, v65, vcc
	v_cmp_le_i32_e32 vcc, v48, v236
	v_or_b32_e32 v48, 0xf8, v235
	v_max3_f32 v68, v68, v61, v44
	v_cndmask_b32_e32 v64, v222, v90, vcc
	v_cmp_le_i32_e32 vcc, v48, v236
	v_max3_f32 v69, v69, v46, v47
	v_max3_f32 v68, v68, v45, v64
	v_cndmask_b32_e32 v48, v222, v66, vcc
	v_cmp_le_i32_e32 vcc, v49, v236
	v_or_b32_e32 v49, 0xf9, v235
	v_add_f32_e32 v2, v241, v2
	v_cndmask_b32_e32 v65, v222, v91, vcc
	v_cmp_le_i32_e32 vcc, v49, v236
	v_max3_f32 v68, v68, v65, v48
	s_nop 0
	v_cndmask_b32_e32 v49, v222, v67, vcc
	v_cmp_le_i32_e32 vcc, v50, v236
	v_or_b32_e32 v50, 0xfa, v235
	s_nop 0
	v_cndmask_b32_e32 v66, v222, v92, vcc
	v_cmp_le_i32_e32 vcc, v50, v236
	s_nop 1
	v_cndmask_b32_e32 v50, v222, v70, vcc
	v_cmp_le_i32_e32 vcc, v51, v236
	v_or_b32_e32 v51, 0xfb, v235
	s_nop 0
	v_cndmask_b32_e32 v67, v222, v93, vcc
	v_cmp_le_i32_e32 vcc, v51, v236
	v_max3_f32 v69, v69, v66, v67
	s_nop 0
	v_cndmask_b32_e32 v51, v222, v71, vcc
	v_max3_f32 v69, v69, v50, v51
	v_max3_f32 v68, v68, v49, v69
	v_mov_b32_e32 v69, v68
	s_nop 1
	v_permlane32_swap_b32_e32 v68, v69
	v_max_f32_e32 v69, v69, v69
	v_max_f32_e32 v68, v68, v68
	v_max_f32_e32 v68, v68, v69
	v_cmp_lt_f32_e32 vcc, s94, v68
	s_cmp_lg_u64 vcc, 0
	s_cselect_b64 s[4:5], -1, 0
	s_cbranch_vccnz .LBB0_1024

; #define SBAR() __builtin_amdgcn_sched_barrier(0)
;   #define PKW(P,B) cvtpk_s(P[B],P[B+1])
;   #define PKW(P,B) cvtpk_s(P[B],P[B+1])
; __device__ __forceinline__ void pv(f32x16*o,int vb,bf16x8 pa0,bf16x8 pa1,bf16x8 pa2,bf16x8 pa3){
;   #pragma unroll
;   for(int d0=0;d0<2;++d0){s16x4 lo[4],hi[4];
;     #pragma unroll
;     for(int ks=0;ks<4;++ks){
;       asm volatile("ds_read_b64_tr_b16 %0,%1 offset:%c2":"=&v"(lo[ks]):"v"(vb),"i"(d0*4096+ks*1024):"memory");
;       asm volatile("ds_read_b64_tr_b16 %0,%1 offset:%c2":"=&v"(hi[ks]):"v"(vb),"i"(d0*4096+ks*1024+512):"memory");}
;     asm volatile("s_waitcnt lgkmcnt(0)":::"memory");SBAR();
;     ...
;     o[d0]=__builtin_amdgcn_mfma_f32_32x32x16_bf16(pa0,PK(0),o[d0],0,0,0);
;     o[d0]=__builtin_amdgcn_mfma_f32_32x32x16_bf16(pa1,PK(1),o[d0],0,0,0);
;     o[d0]=__builtin_amdgcn_mfma_f32_32x32x16_bf16(pa2,PK(2),o[d0],0,0,0);
;     o[d0]=__builtin_amdgcn_mfma_f32_32x32x16_bf16(pa3,PK(3),o[d0],0,0,0);
;     ...
;   }
;     ...
;   { float sacc=pB0[0]+pB0[1]; _Pragma("unroll") for(int r=2;r<16;++r)sacc+=pB0[r]; _Pragma("unroll") for(int r=0;r<16;++r)sacc+=pB1[r]; l_reg+=sacc;
;     pw0=(u32x4){PKW(pB0,0),PKW(pB0,2),PKW(pB0,4),PKW(pB0,6)};pw1=(u32x4){PKW(pB0,8),PKW(pB0,10),PKW(pB0,12),PKW(pB0,14)};pw2=(u32x4){PKW(pB1,0),PKW(pB1,2),PKW(pB1,4),PKW(pB1,6)};pw3=(u32x4){PKW(pB1,8),PKW(pB1,10),PKW(pB1,12),PKW(pB1,14)};
;     SBAR(); pv(o,vb0+sl_cur,PAF(0),PAF(1),PAF(2),PAF(3)); }
;     ...
;   {auto rr=__builtin_amdgcn_permlane32_swap(__float_as_uint(l_reg),__float_as_uint(l_reg),false,false);l_reg=__uint_as_float(rr[0])+__uint_as_float(rr[1]);}
;   if(hi==0)wsf[32+r32]=l_reg;asm volatile("s_waitcnt lgkmcnt(0)":::"memory");
.LBB0_972:
	v_add_f32_e32 v254, v52, v53
	v_add_f32_e32 v255, v54, v55
	v_add_f32_e32 v254, v56, v254
	v_add_f32_e32 v255, v57, v255
	v_add_f32_e32 v254, v58, v254
	v_add_f32_e32 v255, v59, v255
	v_add_f32_e32 v254, v60, v254
	v_add_f32_e32 v255, v61, v255
	v_add_f32_e32 v254, v62, v254
	v_add_f32_e32 v255, v63, v255
	v_add_f32_e32 v254, v64, v254
	v_add_f32_e32 v255, v65, v255
	v_add_f32_e32 v254, v66, v254
	v_add_f32_e32 v255, v67, v255
	v_add_f32_e32 v254, v36, v254
	v_add_f32_e32 v255, v37, v255
	v_add_f32_e32 v254, v38, v254
	v_add_f32_e32 v255, v39, v255
	v_add_f32_e32 v254, v40, v254
	v_add_f32_e32 v255, v41, v255
	v_add_f32_e32 v254, v42, v254
	v_add_f32_e32 v255, v43, v255
	v_add_f32_e32 v254, v44, v254
	v_add_f32_e32 v255, v45, v255
	v_add_f32_e32 v254, v46, v254
	v_add_f32_e32 v255, v47, v255
	v_add_f32_e32 v254, v48, v254
	v_add_f32_e32 v255, v49, v255
	s_cmp_lg_u32 0, -1
	v_add_f32_e32 v254, v50, v254
	s_cselect_b32 s4, 0, 0
	v_add_f32_e32 v255, v51, v255
	v_add_f32_e32 v69, v254, v255
	s_addk_i32 s4, 0x6000
	v_add_f32_e32 v2, v2, v69
	v_cvt_pk_bf16_f32 v36, v36, v37
	v_add3_u32 v68, v234, s4, v231
	v_cvt_pk_bf16_f32 v52, v52, v53
	v_cvt_pk_bf16_f32 v53, v54, v55
	v_cvt_pk_bf16_f32 v54, v56, v57
	v_cvt_pk_bf16_f32 v55, v58, v59
	v_cvt_pk_bf16_f32 v56, v60, v61
	v_cvt_pk_bf16_f32 v57, v62, v63
	v_cvt_pk_bf16_f32 v58, v64, v65
	v_cvt_pk_bf16_f32 v59, v66, v67
	v_cvt_pk_bf16_f32 v37, v38, v39
	v_cvt_pk_bf16_f32 v38, v40, v41
	v_cvt_pk_bf16_f32 v39, v42, v43
	v_cvt_pk_bf16_f32 v40, v44, v45
	v_cvt_pk_bf16_f32 v41, v46, v47
	v_cvt_pk_bf16_f32 v42, v48, v49
	v_cvt_pk_bf16_f32 v43, v50, v51
	v_add3_u32 v68, v68, v232, s61
	ds_read_b64_tr_b16 v[44:45],v68 offset:0
	ds_read_b64_tr_b16 v[46:47],v68 offset:512
	ds_read_b64_tr_b16 v[48:49],v68 offset:1024
	ds_read_b64_tr_b16 v[50:51],v68 offset:1536
	ds_read_b64_tr_b16 v[60:61],v68 offset:2048
	ds_read_b64_tr_b16 v[62:63],v68 offset:2560
	ds_read_b64_tr_b16 v[64:65],v68 offset:3072
	ds_read_b64_tr_b16 v[66:67],v68 offset:3584
	s_waitcnt lgkmcnt(0)
	s_nop 0
	v_mfma_f32_32x32x16_bf16 v[20:35], v[52:55], v[44:47], v[20:35]
	ds_read_b64_tr_b16 v[44:45],v68 offset:4096
	ds_read_b64_tr_b16 v[46:47],v68 offset:4608
	v_mfma_f32_32x32x16_bf16 v[20:35], v[56:59], v[48:51], v[20:35]
	ds_read_b64_tr_b16 v[48:49],v68 offset:5120
	ds_read_b64_tr_b16 v[50:51],v68 offset:5632
	v_mfma_f32_32x32x16_bf16 v[20:35], v[36:39], v[60:63], v[20:35]
	ds_read_b64_tr_b16 v[60:61],v68 offset:6144
	ds_read_b64_tr_b16 v[62:63],v68 offset:6656
	v_mfma_f32_32x32x16_bf16 v[20:35], v[40:43], v[64:67], v[20:35]
	ds_read_b64_tr_b16 v[64:65],v68 offset:7168
	ds_read_b64_tr_b16 v[66:67],v68 offset:7680
	s_waitcnt lgkmcnt(0)
	v_mfma_f32_32x32x16_bf16 v[4:19], v[52:55], v[44:47], v[4:19]
	v_cmp_gt_u32_e32 vcc, 32, v227
	v_mfma_f32_32x32x16_bf16 v[4:19], v[56:59], v[48:51], v[4:19]
	v_mfma_f32_32x32x16_bf16 v[4:19], v[36:39], v[60:63], v[4:19]
	v_mov_b32_e32 v36, v2
	s_nop 1
	v_permlane32_swap_b32_e32 v2, v36
	v_mfma_f32_32x32x16_bf16 v[4:19], v[40:43], v[64:67], v[4:19]
	s_and_saveexec_b64 s[4:5], vcc
	s_cbranch_execz .LBB0_930
	v_lshl_add_u32 v37, v229, 2, s56
	v_add_f32_e32 v2, v2, v36
	ds_write_b32 v37, v2 offset:49280
	s_branch .LBB0_930

.LBB0_976:
	v_add_u32_e32 v2, s7, v240
	ds_read_b64_tr_b16 v[176:177], v2 offset:24576
	ds_read_b64_tr_b16 v[178:179], v2 offset:25088
	s_waitcnt lgkmcnt(3)
	v_mfma_f32_32x32x16_bf16 v[84:99], v[160:163], v[116:119], 0
	v_add_f32_e32 v254, v52, v53
	v_add_f32_e32 v255, v54, v55
	v_add_f32_e32 v254, v56, v254
	v_add_f32_e32 v255, v57, v255
	v_cvt_pk_bf16_f32 v128, v52, v53
	v_cvt_pk_bf16_f32 v129, v54, v55
	ds_read_b64_tr_b16 v[160:161], v2 offset:28672
	ds_read_b64_tr_b16 v[162:163], v2 offset:29184
	v_add_f32_e32 v254, v58, v254
	s_waitcnt lgkmcnt(4)
	v_mfma_f32_32x32x16_bf16 v[68:83], v[152:155], v[116:119], 0
	v_add_f32_e32 v255, v59, v255
	v_add_f32_e32 v254, v60, v254
	v_add_f32_e32 v255, v61, v255
	v_cvt_pk_bf16_f32 v130, v56, v57
	v_cvt_pk_bf16_f32 v131, v58, v59
	ds_read_b64_tr_b16 v[164:165], v2 offset:25600
	ds_read_b64_tr_b16 v[166:167], v2 offset:26112
	s_waitcnt lgkmcnt(11)
	v_mfma_f32_32x32x16_bf16 v[84:99], v[156:159], v[108:111], v[84:99]
	v_add_f32_e32 v254, v62, v254
	v_add_f32_e32 v255, v63, v255
	v_add_f32_e32 v254, v64, v254
	v_add_f32_e32 v255, v65, v255
	v_cvt_pk_bf16_f32 v124, v60, v61
	v_cvt_pk_bf16_f32 v125, v62, v63
	ds_read_b64_tr_b16 v[168:169], v2 offset:29696
	ds_read_b64_tr_b16 v[170:171], v2 offset:30208
	s_waitcnt lgkmcnt(12)
	v_mfma_f32_32x32x16_bf16 v[68:83], v[148:151], v[108:111], v[68:83]
	v_add_f32_e32 v254, v66, v254
	v_add_f32_e32 v255, v67, v255
	v_add_f32_e32 v254, v36, v254
	v_add_f32_e32 v255, v37, v255
	v_cvt_pk_bf16_f32 v126, v64, v65
	v_cvt_pk_bf16_f32 v127, v66, v67
	ds_read_b64_tr_b16 v[172:173], v2 offset:26624
	ds_read_b64_tr_b16 v[174:175], v2 offset:27136
	s_waitcnt lgkmcnt(13)
	v_mfma_f32_32x32x16_bf16 v[84:99], v[144:147], v[104:107], v[84:99]
	v_add_f32_e32 v254, v38, v254
	v_add_f32_e32 v255, v39, v255
	v_add_f32_e32 v254, v40, v254
	v_add_f32_e32 v255, v41, v255
	v_cvt_pk_bf16_f32 v120, v36, v37
	v_cvt_pk_bf16_f32 v121, v38, v39
	ds_read_b64_tr_b16 v[180:181], v2 offset:30720
	ds_read_b64_tr_b16 v[182:183], v2 offset:31232
	s_waitcnt lgkmcnt(14)
	v_mfma_f32_32x32x16_bf16 v[68:83], v[140:143], v[104:107], v[68:83]
	v_add_f32_e32 v254, v42, v254
	v_add_f32_e32 v255, v43, v255
	v_add_f32_e32 v254, v44, v254
	v_add_f32_e32 v255, v45, v255
	v_cvt_pk_bf16_f32 v122, v40, v41
	v_cvt_pk_bf16_f32 v123, v42, v43
	ds_read_b64_tr_b16 v[184:185], v2 offset:27648
	ds_read_b64_tr_b16 v[186:187], v2 offset:28160
	s_waitcnt lgkmcnt(14)
	v_mfma_f32_32x32x16_bf16 v[84:99], v[136:139], v[100:103], v[84:99]
	v_add_f32_e32 v254, v46, v254
	v_add_f32_e32 v255, v47, v255
	v_add_f32_e32 v254, v48, v254
	v_add_f32_e32 v255, v49, v255
	v_cvt_pk_bf16_f32 v112, v44, v45
	v_cvt_pk_bf16_f32 v113, v46, v47
	ds_read_b64_tr_b16 v[188:189], v2 offset:31744
	ds_read_b64_tr_b16 v[190:191], v2 offset:32256
	v_mfma_f32_32x32x16_bf16 v[68:83], v[132:135], v[100:103], v[68:83]
	v_add_f32_e32 v254, v50, v254
	v_add_f32_e32 v255, v51, v255
	v_add_f32_e32 v2, v254, v255
	v_add_f32_e32 v2, 0, v2
	v_cvt_pk_bf16_f32 v114, v48, v49
	v_cvt_pk_bf16_f32 v115, v50, v51
	s_add_i32 s6, s34, 1
	s_cmp_ge_i32 s6, s60
	s_cselect_b64 s[26:27], -1, 0
	s_and_b64 vcc, exec, s[26:27]
	s_cbranch_vccnz .LBB0_978
	v_lshl_add_u64 v[36:37], v[196:197], 0, s[18:19]
	s_mov_b64 s[6:7], 0x13060000
	s_add_i32 s28, s61, s58
	v_lshl_add_u64 v[36:37], v[36:37], 0, s[6:7]
	s_mov_b32 s6, m0
	s_mov_b32 m0, s28
	s_nop 0
	global_load_lds_dwordx4 v[36:37], off
	s_mov_b32 m0, s6

.LBB0_985:
	v_add_u32_e32 v166, s61, v240
	ds_read_b64_tr_b16 v[192:193], v166 offset:24576
	ds_read_b64_tr_b16 v[194:195], v166 offset:25088
	s_waitcnt lgkmcnt(9)
	v_mfma_f32_32x32x16_bf16 v[84:99], v[160:163], v[116:119], 0
	v_add_f32_e32 v254, v52, v53
	v_add_f32_e32 v255, v54, v55
	v_add_f32_e32 v254, v56, v254
	v_add_f32_e32 v255, v57, v255
	v_cvt_pk_bf16_f32 v128, v52, v53
	v_cvt_pk_bf16_f32 v129, v54, v55
	ds_read_b64_tr_b16 v[188:189], v166 offset:28672
	ds_read_b64_tr_b16 v[190:191], v166 offset:29184
	v_add_f32_e32 v254, v58, v254
	s_waitcnt lgkmcnt(10)
	v_mfma_f32_32x32x16_bf16 v[68:83], v[152:155], v[116:119], 0
	v_add_f32_e32 v255, v59, v255
	v_add_f32_e32 v254, v60, v254
	v_add_f32_e32 v255, v61, v255
	v_cvt_pk_bf16_f32 v130, v56, v57
	v_cvt_pk_bf16_f32 v131, v58, v59
	ds_read_b64_tr_b16 v[184:185], v166 offset:25600
	ds_read_b64_tr_b16 v[186:187], v166 offset:26112
	s_waitcnt lgkmcnt(11)
	v_mfma_f32_32x32x16_bf16 v[84:99], v[156:159], v[108:111], v[84:99]
	v_add_f32_e32 v254, v62, v254
	v_add_f32_e32 v255, v63, v255
	v_add_f32_e32 v254, v64, v254
	v_add_f32_e32 v255, v65, v255
	v_cvt_pk_bf16_f32 v124, v60, v61
	v_cvt_pk_bf16_f32 v125, v62, v63
	ds_read_b64_tr_b16 v[180:181], v166 offset:29696
	ds_read_b64_tr_b16 v[182:183], v166 offset:30208
	s_waitcnt lgkmcnt(12)
	v_mfma_f32_32x32x16_bf16 v[68:83], v[148:151], v[108:111], v[68:83]
	v_add_f32_e32 v254, v66, v254
	v_add_f32_e32 v255, v67, v255
	v_add_f32_e32 v254, v36, v254
	v_add_f32_e32 v255, v37, v255
	v_cvt_pk_bf16_f32 v126, v64, v65
	v_cvt_pk_bf16_f32 v127, v66, v67
	ds_read_b64_tr_b16 v[176:177], v166 offset:26624
	ds_read_b64_tr_b16 v[178:179], v166 offset:27136
	s_waitcnt lgkmcnt(13)
	v_mfma_f32_32x32x16_bf16 v[84:99], v[144:147], v[104:107], v[84:99]
	v_add_f32_e32 v254, v38, v254
	v_add_f32_e32 v255, v39, v255
	v_add_f32_e32 v254, v40, v254
	v_add_f32_e32 v255, v41, v255
	v_cvt_pk_bf16_f32 v120, v36, v37
	v_cvt_pk_bf16_f32 v121, v38, v39
	ds_read_b64_tr_b16 v[172:173], v166 offset:30720
	ds_read_b64_tr_b16 v[174:175], v166 offset:31232
	s_waitcnt lgkmcnt(14)
	v_mfma_f32_32x32x16_bf16 v[68:83], v[140:143], v[104:107], v[68:83]
	v_add_f32_e32 v254, v42, v254
	v_add_f32_e32 v255, v43, v255
	v_add_f32_e32 v254, v44, v254
	v_add_f32_e32 v255, v45, v255
	v_cvt_pk_bf16_f32 v122, v40, v41
	v_cvt_pk_bf16_f32 v123, v42, v43
	ds_read_b64_tr_b16 v[168:169], v166 offset:27648
	ds_read_b64_tr_b16 v[170:171], v166 offset:28160
	s_waitcnt lgkmcnt(14)
	v_mfma_f32_32x32x16_bf16 v[84:99], v[136:139], v[100:103], v[84:99]
	v_add_f32_e32 v254, v46, v254
	v_add_f32_e32 v255, v47, v255
	v_add_f32_e32 v254, v48, v254
	v_add_f32_e32 v255, v49, v255
	v_cvt_pk_bf16_f32 v112, v44, v45
	v_cvt_pk_bf16_f32 v113, v46, v47
	ds_read_b64_tr_b16 v[164:165], v166 offset:31744
	ds_read_b64_tr_b16 v[166:167], v166 offset:32256
	v_mfma_f32_32x32x16_bf16 v[68:83], v[132:135], v[100:103], v[68:83]
	v_add_f32_e32 v254, v50, v254
	v_add_f32_e32 v255, v51, v255
	v_add_f32_e32 v36, v254, v255
	v_add_f32_e32 v241, 0, v36
	v_cvt_pk_bf16_f32 v114, v48, v49
	v_cvt_pk_bf16_f32 v115, v50, v51
	s_add_i32 s64, s34, 2
	s_cmp_ge_i32 s64, s60
	s_cselect_b64 s[28:29], -1, 0
	s_and_b64 vcc, exec, s[28:29]
	s_cbranch_vccnz .LBB0_987
	v_lshl_add_u64 v[36:37], v[196:197], 0, s[18:19]
	s_mov_b64 s[30:31], 0x13080000
	s_add_i32 s6, s38, s58
	v_lshl_add_u64 v[36:37], v[36:37], 0, s[30:31]
	s_mov_b32 s7, m0
	s_mov_b32 m0, s6
	s_nop 0
	global_load_lds_dwordx4 v[36:37], off
	s_mov_b32 m0, s7

.LBB0_1425:
	v_add_u32_e32 v170, s72, v239
	ds_read_b64_tr_b16 v[166:167], v170 offset:24576
	ds_read_b64_tr_b16 v[168:169], v170 offset:25088
	v_add_f32_e32 v254, v52, v53
	v_add_f32_e32 v255, v54, v55
	v_cvt_pk_bf16_f32 v52, v52, v53
	v_add_f32_e32 v254, v56, v254
	v_cndmask_b32_e64 v130, 0, v52, s[92:93]
	v_cvt_pk_bf16_f32 v52, v54, v55
	v_add_f32_e32 v255, v57, v255
	v_cndmask_b32_e64 v131, 0, v52, s[92:93]
	s_waitcnt lgkmcnt(9)
	v_mfma_f32_32x32x16_bf16 v[68:83], v[162:165], v[126:129], 0
	ds_read_b64_tr_b16 v[162:163], v170 offset:28672
	ds_read_b64_tr_b16 v[164:165], v170 offset:29184
	v_add_f32_e32 v254, v58, v254
	v_add_f32_e32 v255, v59, v255
	v_cvt_pk_bf16_f32 v53, v56, v57
	v_add_f32_e32 v254, v60, v254
	v_cndmask_b32_e64 v132, 0, v53, s[92:93]
	v_cvt_pk_bf16_f32 v53, v58, v59
	v_add_f32_e32 v255, v61, v255
	v_cndmask_b32_e64 v133, 0, v53, s[92:93]
	s_waitcnt lgkmcnt(10)
	v_mfma_f32_32x32x16_bf16 v[84:99], v[154:157], v[126:129], 0
	ds_read_b64_tr_b16 v[154:155], v170 offset:25600
	ds_read_b64_tr_b16 v[156:157], v170 offset:26112
	v_add_f32_e32 v254, v62, v254
	v_add_f32_e32 v255, v63, v255
	v_cvt_pk_bf16_f32 v53, v60, v61
	v_add_f32_e32 v254, v64, v254
	v_cndmask_b32_e64 v108, 0, v53, s[92:93]
	v_cvt_pk_bf16_f32 v53, v62, v63
	v_add_f32_e32 v255, v65, v255
	v_cndmask_b32_e64 v109, 0, v53, s[92:93]
	s_waitcnt lgkmcnt(11)
	v_mfma_f32_32x32x16_bf16 v[68:83], v[158:161], v[122:125], v[68:83]
	ds_read_b64_tr_b16 v[158:159], v170 offset:29696
	ds_read_b64_tr_b16 v[160:161], v170 offset:30208
	v_add_f32_e32 v254, v66, v254
	v_add_f32_e32 v255, v67, v255
	v_cvt_pk_bf16_f32 v53, v64, v65
	v_add_f32_e32 v254, v36, v254
	v_cndmask_b32_e64 v110, 0, v53, s[92:93]
	v_cvt_pk_bf16_f32 v53, v66, v67
	v_add_f32_e32 v255, v37, v255
	v_cndmask_b32_e64 v111, 0, v53, s[92:93]
	s_waitcnt lgkmcnt(12)
	v_mfma_f32_32x32x16_bf16 v[84:99], v[150:153], v[122:125], v[84:99]
	ds_read_b64_tr_b16 v[150:151], v170 offset:26624
	ds_read_b64_tr_b16 v[152:153], v170 offset:27136
	v_add_f32_e32 v254, v38, v254
	v_add_f32_e32 v255, v39, v255
	v_cvt_pk_bf16_f32 v36, v36, v37
	v_add_f32_e32 v254, v40, v254
	v_cndmask_b32_e64 v104, 0, v36, s[92:93]
	v_cvt_pk_bf16_f32 v36, v38, v39
	v_add_f32_e32 v255, v41, v255
	v_cndmask_b32_e64 v105, 0, v36, s[92:93]
	s_waitcnt lgkmcnt(13)
	v_mfma_f32_32x32x16_bf16 v[68:83], v[146:149], v[118:121], v[68:83]
	ds_read_b64_tr_b16 v[146:147], v170 offset:30720
	ds_read_b64_tr_b16 v[148:149], v170 offset:31232
	v_add_f32_e32 v254, v42, v254
	v_add_f32_e32 v255, v43, v255
	v_cvt_pk_bf16_f32 v37, v40, v41
	v_add_f32_e32 v254, v44, v254
	v_cndmask_b32_e64 v106, 0, v37, s[92:93]
	v_cvt_pk_bf16_f32 v37, v42, v43
	v_add_f32_e32 v255, v45, v255
	v_cndmask_b32_e64 v107, 0, v37, s[92:93]
	s_waitcnt lgkmcnt(14)
	v_mfma_f32_32x32x16_bf16 v[84:99], v[142:145], v[118:121], v[84:99]
	ds_read_b64_tr_b16 v[142:143], v170 offset:27648
	ds_read_b64_tr_b16 v[144:145], v170 offset:28160
	v_add_f32_e32 v254, v46, v254
	v_add_f32_e32 v255, v47, v255
	v_cvt_pk_bf16_f32 v37, v44, v45
	v_add_f32_e32 v254, v48, v254
	v_cndmask_b32_e64 v100, 0, v37, s[92:93]
	v_cvt_pk_bf16_f32 v37, v46, v47
	v_add_f32_e32 v255, v49, v255
	v_cndmask_b32_e64 v101, 0, v37, s[92:93]
	s_waitcnt lgkmcnt(14)
	v_mfma_f32_32x32x16_bf16 v[68:83], v[138:141], v[114:117], v[68:83]
	ds_read_b64_tr_b16 v[138:139], v170 offset:31744
	ds_read_b64_tr_b16 v[140:141], v170 offset:32256
	v_add_f32_e32 v254, v50, v254
	v_add_f32_e32 v255, v51, v255
	v_add_f32_e32 v36, v254, v255
	v_mfma_f32_32x32x16_bf16 v[84:99], v[134:137], v[114:117], v[84:99]
	v_add_f32_e32 v134, 0, v36
	v_cvt_pk_bf16_f32 v36, v48, v49
	v_cndmask_b32_e64 v102, 0, v36, s[92:93]
	v_cvt_pk_bf16_f32 v36, v50, v51
	v_cndmask_b32_e64 v103, 0, v36, s[92:93]
	v_mov_b32_e32 v36, s85
	ds_read_b32 v37, v36 offset:12
	v_pk_add_f32 v[52:53], v[68:69], v[2:3] op_sel_hi:[1,0] neg_lo:[0,1] neg_hi:[0,1]
	v_pk_add_f32 v[54:55], v[70:71], v[2:3] op_sel_hi:[1,0] neg_lo:[0,1] neg_hi:[0,1]
	s_nop 2
	v_pk_add_f32 v[38:39], v[86:87], v[2:3] op_sel_hi:[1,0] neg_lo:[0,1] neg_hi:[0,1]
	v_pk_add_f32 v[56:57], v[72:73], v[2:3] op_sel_hi:[1,0] neg_lo:[0,1] neg_hi:[0,1]
	s_waitcnt lgkmcnt(0)
	v_readfirstlane_b32 s4, v37
	s_lshl_b32 s4, s4, 13
	s_and_b32 s4, s4, 0x7e000
	s_add_u32 s72, s77, s4
	s_addc_u32 s73, s78, 0
	s_add_i32 s4, s91, s95
	s_mov_b32 s76, m0
	s_mov_b32 m0, s4
	s_nop 0
	global_load_lds_dwordx4 v236, s[72:73]
	s_mov_b32 m0, s76
	ds_read_b32 v37, v36 offset:4
	v_pk_add_f32 v[40:41], v[88:89], v[2:3] op_sel_hi:[1,0] neg_lo:[0,1] neg_hi:[0,1]
	v_pk_add_f32 v[58:59], v[74:75], v[2:3] op_sel_hi:[1,0] neg_lo:[0,1] neg_hi:[0,1]
	v_pk_add_f32 v[42:43], v[90:91], v[2:3] op_sel_hi:[1,0] neg_lo:[0,1] neg_hi:[0,1]
	v_pk_add_f32 v[60:61], v[76:77], v[2:3] op_sel_hi:[1,0] neg_lo:[0,1] neg_hi:[0,1]
	s_waitcnt lgkmcnt(0)
	v_readfirstlane_b32 s4, v37
	s_lshl_b32 s4, s4, 13
	s_and_b32 s4, s4, 0x7e000
	s_add_u32 s72, s79, s4
	s_addc_u32 s73, s88, 0
	s_add_i32 s4, s90, s75
	s_mov_b32 s76, m0
	s_mov_b32 m0, s4
	s_nop 0
	global_load_lds_dwordx4 v237, s[72:73]
	s_mov_b32 m0, s76
	ds_read_b32 v36, v36
	v_pk_add_f32 v[44:45], v[92:93], v[2:3] op_sel_hi:[1,0] neg_lo:[0,1] neg_hi:[0,1]
	v_pk_add_f32 v[62:63], v[78:79], v[2:3] op_sel_hi:[1,0] neg_lo:[0,1] neg_hi:[0,1]
	v_pk_add_f32 v[46:47], v[94:95], v[2:3] op_sel_hi:[1,0] neg_lo:[0,1] neg_hi:[0,1]
	v_pk_add_f32 v[64:65], v[80:81], v[2:3] op_sel_hi:[1,0] neg_lo:[0,1] neg_hi:[0,1]
	s_waitcnt lgkmcnt(0)
	v_readfirstlane_b32 s4, v36
	s_and_b32 s72, s4, 63
	s_sub_i32 s73, s94, s72
	v_pk_add_f32 v[36:37], v[84:85], v[2:3] op_sel_hi:[1,0] neg_lo:[0,1] neg_hi:[0,1]
	v_pk_add_f32 v[48:49], v[96:97], v[2:3] op_sel_hi:[1,0] neg_lo:[0,1] neg_hi:[0,1]
	v_pk_add_f32 v[66:67], v[82:83], v[2:3] op_sel_hi:[1,0] neg_lo:[0,1] neg_hi:[0,1]
	v_pk_add_f32 v[50:51], v[98:99], v[2:3] op_sel_hi:[1,0] neg_lo:[0,1] neg_hi:[0,1]
	s_cmp_gt_i32 s73, 2
	s_cbranch_scc1 .LBB0_1427
	v_lshl_add_u32 v99, s73, 8, v183
	ds_read_b32 v68, v99 offset:256
	ds_read_b32 v70, v99 offset:128
	ds_read_b32 v69, v99 offset:252
	ds_read_b32 v71, v99 offset:124
	ds_read_b32 v72, v99 offset:248
	ds_read_b32 v74, v99 offset:120
	ds_read_b32 v73, v99 offset:244
	ds_read_b32 v75, v99 offset:116
	ds_read_b32 v76, v99 offset:224
	ds_read_b32 v78, v99 offset:96
	ds_read_b32 v77, v99 offset:220
	ds_read_b32 v79, v99 offset:92
	ds_read_b32 v80, v99 offset:216
	ds_read_b32 v82, v99 offset:88
	ds_read_b32 v81, v99 offset:212
	ds_read_b32 v83, v99 offset:84
	ds_read_b32 v84, v99 offset:192
	ds_read_b32 v86, v99 offset:64
	ds_read_b32 v85, v99 offset:188
	ds_read_b32 v87, v99 offset:60
	ds_read_b32 v88, v99 offset:184
	ds_read_b32 v90, v99 offset:56
	ds_read_b32 v89, v99 offset:180
	ds_read_b32 v91, v99 offset:52
	ds_read_b32 v92, v99 offset:160
	ds_read_b32 v94, v99 offset:32
	ds_read_b32 v93, v99 offset:156
	ds_read_b32 v95, v99 offset:28
	ds_read_b32 v96, v99 offset:152
	ds_read_b32 v98, v99 offset:24
	ds_read_b32 v97, v99 offset:148
	ds_read_b32 v99, v99 offset:20
	s_waitcnt lgkmcnt(14)
	v_pk_add_f32 v[52:53], v[52:53], v[68:69]
	v_pk_add_f32 v[54:55], v[54:55], v[72:73]
	v_pk_add_f32 v[56:57], v[56:57], v[76:77]
	v_pk_add_f32 v[58:59], v[58:59], v[80:81]
	s_waitcnt lgkmcnt(13)
	v_pk_add_f32 v[60:61], v[60:61], v[84:85]
	s_waitcnt lgkmcnt(9)
	v_pk_add_f32 v[62:63], v[62:63], v[88:89]
	s_waitcnt lgkmcnt(5)
	v_pk_add_f32 v[64:65], v[64:65], v[92:93]
	s_waitcnt lgkmcnt(1)
	v_pk_add_f32 v[66:67], v[66:67], v[96:97]
	v_pk_add_f32 v[36:37], v[36:37], v[70:71]
	v_pk_add_f32 v[38:39], v[38:39], v[74:75]
	v_pk_add_f32 v[40:41], v[40:41], v[78:79]
	v_pk_add_f32 v[42:43], v[42:43], v[82:83]
	v_pk_add_f32 v[44:45], v[44:45], v[86:87]
	v_pk_add_f32 v[46:47], v[46:47], v[90:91]
	v_pk_add_f32 v[48:49], v[48:49], v[94:95]
	s_waitcnt lgkmcnt(0)
	v_pk_add_f32 v[50:51], v[50:51], v[98:99]

.LBB0_1432:
	s_add_i32 s4, s90, 0x2000
	s_cmpk_lg_i32 s90, 0x4000
	s_cselect_b32 s84, s4, 0
	v_add_u32_e32 v180, s91, v239
	ds_read_b64_tr_b16 v[138:139], v180 offset:24576
	ds_read_b64_tr_b16 v[140:141], v180 offset:25088
	v_add_f32_e32 v254, v52, v53
	v_add_f32_e32 v255, v54, v55
	v_cvt_pk_bf16_f32 v52, v52, v53
	v_add_f32_e32 v254, v56, v254
	v_cndmask_b32_e64 v130, 0, v52, s[72:73]
	v_cvt_pk_bf16_f32 v52, v54, v55
	v_add_f32_e32 v255, v57, v255
	v_cndmask_b32_e64 v131, 0, v52, s[72:73]
	s_waitcnt lgkmcnt(9)
	v_mfma_f32_32x32x16_bf16 v[68:83], v[68:71], v[126:129], 0
	ds_read_b64_tr_b16 v[142:143], v180 offset:28672
	ds_read_b64_tr_b16 v[144:145], v180 offset:29184
	v_add_f32_e32 v254, v58, v254
	v_add_f32_e32 v255, v59, v255
	v_cvt_pk_bf16_f32 v53, v56, v57
	v_add_f32_e32 v254, v60, v254
	v_cndmask_b32_e64 v132, 0, v53, s[72:73]
	v_cvt_pk_bf16_f32 v53, v58, v59
	v_add_f32_e32 v255, v61, v255
	v_cndmask_b32_e64 v133, 0, v53, s[72:73]
	s_waitcnt lgkmcnt(10)
	v_mfma_f32_32x32x16_bf16 v[84:99], v[84:87], v[126:129], 0
	ds_read_b64_tr_b16 v[134:135], v180 offset:25600
	ds_read_b64_tr_b16 v[136:137], v180 offset:26112
	v_add_f32_e32 v254, v62, v254
	v_add_f32_e32 v255, v63, v255
	v_cvt_pk_bf16_f32 v53, v60, v61
	v_add_f32_e32 v254, v64, v254
	v_cndmask_b32_e64 v108, 0, v53, s[72:73]
	v_cvt_pk_bf16_f32 v53, v62, v63
	v_add_f32_e32 v255, v65, v255
	v_cndmask_b32_e64 v109, 0, v53, s[72:73]
	s_waitcnt lgkmcnt(11)
	v_mfma_f32_32x32x16_bf16 v[68:83], v[170:173], v[122:125], v[68:83]
	ds_read_b64_tr_b16 v[146:147], v180 offset:29696
	ds_read_b64_tr_b16 v[148:149], v180 offset:30208
	v_add_f32_e32 v254, v66, v254
	v_add_f32_e32 v255, v67, v255
	v_cvt_pk_bf16_f32 v53, v64, v65
	v_add_f32_e32 v254, v36, v254
	v_cndmask_b32_e64 v110, 0, v53, s[72:73]
	v_cvt_pk_bf16_f32 v53, v66, v67
	v_add_f32_e32 v255, v37, v255
	v_cndmask_b32_e64 v111, 0, v53, s[72:73]
	s_waitcnt lgkmcnt(12)
	v_mfma_f32_32x32x16_bf16 v[84:99], v[166:169], v[122:125], v[84:99]
	ds_read_b64_tr_b16 v[166:167], v180 offset:26624
	ds_read_b64_tr_b16 v[168:169], v180 offset:27136
	v_add_f32_e32 v254, v38, v254
	v_add_f32_e32 v255, v39, v255
	v_cvt_pk_bf16_f32 v36, v36, v37
	v_add_f32_e32 v254, v40, v254
	v_cndmask_b32_e64 v104, 0, v36, s[72:73]
	v_cvt_pk_bf16_f32 v36, v38, v39
	v_add_f32_e32 v255, v41, v255
	v_cndmask_b32_e64 v105, 0, v36, s[72:73]
	s_waitcnt lgkmcnt(13)
	v_mfma_f32_32x32x16_bf16 v[68:83], v[162:165], v[118:121], v[68:83]
	ds_read_b64_tr_b16 v[170:171], v180 offset:30720
	ds_read_b64_tr_b16 v[172:173], v180 offset:31232
	v_add_f32_e32 v254, v42, v254
	v_add_f32_e32 v255, v43, v255
	v_cvt_pk_bf16_f32 v37, v40, v41
	v_add_f32_e32 v254, v44, v254
	v_cndmask_b32_e64 v106, 0, v37, s[72:73]
	v_cvt_pk_bf16_f32 v37, v42, v43
	v_add_f32_e32 v255, v45, v255
	v_cndmask_b32_e64 v107, 0, v37, s[72:73]
	s_waitcnt lgkmcnt(14)
	v_mfma_f32_32x32x16_bf16 v[84:99], v[158:161], v[118:121], v[84:99]
	ds_read_b64_tr_b16 v[174:175], v180 offset:27648
	ds_read_b64_tr_b16 v[176:177], v180 offset:28160
	v_add_f32_e32 v254, v46, v254
	v_add_f32_e32 v255, v47, v255
	v_cvt_pk_bf16_f32 v37, v44, v45
	v_add_f32_e32 v254, v48, v254
	v_cndmask_b32_e64 v100, 0, v37, s[72:73]
	v_cvt_pk_bf16_f32 v37, v46, v47
	v_add_f32_e32 v255, v49, v255
	v_cndmask_b32_e64 v101, 0, v37, s[72:73]
	s_waitcnt lgkmcnt(14)
	v_mfma_f32_32x32x16_bf16 v[68:83], v[154:157], v[114:117], v[68:83]
	ds_read_b64_tr_b16 v[178:179], v180 offset:31744
	ds_read_b64_tr_b16 v[180:181], v180 offset:32256
	v_add_f32_e32 v254, v50, v254
	v_add_f32_e32 v255, v51, v255
	v_add_f32_e32 v36, v254, v255
	v_mfma_f32_32x32x16_bf16 v[84:99], v[150:153], v[114:117], v[84:99]
	v_add_f32_e32 v150, 0, v36
	v_cvt_pk_bf16_f32 v36, v48, v49
	v_cndmask_b32_e64 v102, 0, v36, s[72:73]
	v_cvt_pk_bf16_f32 v36, v50, v51
	v_cndmask_b32_e64 v103, 0, v36, s[72:73]
	v_mov_b32_e32 v36, s85
	ds_read_b32 v37, v36 offset:16
	v_pk_add_f32 v[52:53], v[68:69], v[2:3] op_sel_hi:[1,0] neg_lo:[0,1] neg_hi:[0,1]
	v_pk_add_f32 v[54:55], v[70:71], v[2:3] op_sel_hi:[1,0] neg_lo:[0,1] neg_hi:[0,1]
	s_nop 2
	v_pk_add_f32 v[38:39], v[86:87], v[2:3] op_sel_hi:[1,0] neg_lo:[0,1] neg_hi:[0,1]
	v_pk_add_f32 v[56:57], v[72:73], v[2:3] op_sel_hi:[1,0] neg_lo:[0,1] neg_hi:[0,1]
	s_waitcnt lgkmcnt(0)
	v_readfirstlane_b32 s4, v37
	s_lshl_b32 s4, s4, 13
	s_and_b32 s4, s4, 0x7e000
	s_add_u32 s80, s77, s4
	s_addc_u32 s81, s78, 0
	s_add_i32 s4, s90, s95
	s_mov_b32 s76, m0
	s_mov_b32 m0, s4
	s_nop 0
	global_load_lds_dwordx4 v236, s[80:81]
	s_mov_b32 m0, s76
	ds_read_b32 v37, v36 offset:8
	v_pk_add_f32 v[40:41], v[88:89], v[2:3] op_sel_hi:[1,0] neg_lo:[0,1] neg_hi:[0,1]
	v_pk_add_f32 v[58:59], v[74:75], v[2:3] op_sel_hi:[1,0] neg_lo:[0,1] neg_hi:[0,1]
	v_pk_add_f32 v[42:43], v[90:91], v[2:3] op_sel_hi:[1,0] neg_lo:[0,1] neg_hi:[0,1]
	v_pk_add_f32 v[60:61], v[76:77], v[2:3] op_sel_hi:[1,0] neg_lo:[0,1] neg_hi:[0,1]
	s_waitcnt lgkmcnt(0)
	v_readfirstlane_b32 s4, v37
	s_lshl_b32 s4, s4, 13
	s_and_b32 s4, s4, 0x7e000
	s_add_u32 s80, s79, s4
	s_addc_u32 s81, s88, 0
	s_add_i32 s4, s84, s75
	s_mov_b32 s76, m0
	s_mov_b32 m0, s4
	s_nop 0
	global_load_lds_dwordx4 v237, s[80:81]
	s_mov_b32 m0, s76
	ds_read_b32 v36, v36 offset:4
	v_pk_add_f32 v[44:45], v[92:93], v[2:3] op_sel_hi:[1,0] neg_lo:[0,1] neg_hi:[0,1]
	v_pk_add_f32 v[62:63], v[78:79], v[2:3] op_sel_hi:[1,0] neg_lo:[0,1] neg_hi:[0,1]
	v_pk_add_f32 v[46:47], v[94:95], v[2:3] op_sel_hi:[1,0] neg_lo:[0,1] neg_hi:[0,1]
	v_pk_add_f32 v[64:65], v[80:81], v[2:3] op_sel_hi:[1,0] neg_lo:[0,1] neg_hi:[0,1]
	s_waitcnt lgkmcnt(0)
	v_readfirstlane_b32 s4, v36
	s_and_b32 s76, s4, 63
	s_sub_i32 s80, s94, s76
	v_pk_add_f32 v[36:37], v[84:85], v[2:3] op_sel_hi:[1,0] neg_lo:[0,1] neg_hi:[0,1]
	v_pk_add_f32 v[48:49], v[96:97], v[2:3] op_sel_hi:[1,0] neg_lo:[0,1] neg_hi:[0,1]
	v_pk_add_f32 v[66:67], v[82:83], v[2:3] op_sel_hi:[1,0] neg_lo:[0,1] neg_hi:[0,1]
	v_pk_add_f32 v[50:51], v[98:99], v[2:3] op_sel_hi:[1,0] neg_lo:[0,1] neg_hi:[0,1]
	s_cmp_gt_i32 s80, 2
	s_cbranch_scc1 .LBB0_1434
	v_lshl_add_u32 v99, s80, 8, v183
	ds_read_b32 v68, v99 offset:256
	ds_read_b32 v70, v99 offset:128
	ds_read_b32 v69, v99 offset:252
	ds_read_b32 v71, v99 offset:124
	ds_read_b32 v72, v99 offset:248
	ds_read_b32 v74, v99 offset:120
	ds_read_b32 v73, v99 offset:244
	ds_read_b32 v75, v99 offset:116
	ds_read_b32 v76, v99 offset:224
	ds_read_b32 v78, v99 offset:96
	ds_read_b32 v77, v99 offset:220
	ds_read_b32 v79, v99 offset:92
	ds_read_b32 v80, v99 offset:216
	ds_read_b32 v82, v99 offset:88
	ds_read_b32 v81, v99 offset:212
	ds_read_b32 v83, v99 offset:84
	ds_read_b32 v84, v99 offset:192
	ds_read_b32 v86, v99 offset:64
	ds_read_b32 v85, v99 offset:188
	ds_read_b32 v87, v99 offset:60
	ds_read_b32 v88, v99 offset:184
	ds_read_b32 v90, v99 offset:56
	ds_read_b32 v89, v99 offset:180
	ds_read_b32 v91, v99 offset:52
	ds_read_b32 v92, v99 offset:160
	ds_read_b32 v94, v99 offset:32
	ds_read_b32 v93, v99 offset:156
	ds_read_b32 v95, v99 offset:28
	ds_read_b32 v96, v99 offset:152
	ds_read_b32 v98, v99 offset:24
	ds_read_b32 v97, v99 offset:148
	ds_read_b32 v99, v99 offset:20
	s_waitcnt lgkmcnt(14)
	v_pk_add_f32 v[52:53], v[52:53], v[68:69]
	v_pk_add_f32 v[54:55], v[54:55], v[72:73]
	v_pk_add_f32 v[56:57], v[56:57], v[76:77]
	v_pk_add_f32 v[58:59], v[58:59], v[80:81]
	s_waitcnt lgkmcnt(13)
	v_pk_add_f32 v[60:61], v[60:61], v[84:85]
	s_waitcnt lgkmcnt(9)
	v_pk_add_f32 v[62:63], v[62:63], v[88:89]
	s_waitcnt lgkmcnt(5)
	v_pk_add_f32 v[64:65], v[64:65], v[92:93]
	s_waitcnt lgkmcnt(1)
	v_pk_add_f32 v[66:67], v[66:67], v[96:97]
	v_pk_add_f32 v[36:37], v[36:37], v[70:71]
	v_pk_add_f32 v[38:39], v[38:39], v[74:75]
	v_pk_add_f32 v[40:41], v[40:41], v[78:79]
	v_pk_add_f32 v[42:43], v[42:43], v[82:83]
	v_pk_add_f32 v[44:45], v[44:45], v[86:87]
	v_pk_add_f32 v[46:47], v[46:47], v[90:91]
	v_pk_add_f32 v[48:49], v[48:49], v[94:95]
	s_waitcnt lgkmcnt(0)
	v_pk_add_f32 v[50:51], v[50:51], v[98:99]

.LBB0_1451:
	v_add_u32_e32 v192, s90, v239
	ds_read_b64_tr_b16 v[182:183], v192 offset:24576
	ds_read_b64_tr_b16 v[184:185], v192 offset:25088
	v_add_f32_e32 v254, v52, v53
	v_add_f32_e32 v255, v54, v55
	v_add_f32_e32 v254, v56, v254
	v_add_f32_e32 v255, v57, v255
	s_waitcnt lgkmcnt(3)
	v_mfma_f32_32x32x16_bf16 v[68:83], v[162:165], v[126:129], 0
	v_cvt_pk_bf16_f32 v52, v52, v53
	v_cndmask_b32_e64 v130, 0, v52, s[92:93]
	v_cvt_pk_bf16_f32 v52, v54, v55
	v_cndmask_b32_e64 v131, 0, v52, s[92:93]
	ds_read_b64_tr_b16 v[162:163], v192 offset:28672
	ds_read_b64_tr_b16 v[164:165], v192 offset:29184
	v_add_f32_e32 v254, v58, v254
	s_waitcnt lgkmcnt(4)
	v_mfma_f32_32x32x16_bf16 v[84:99], v[154:157], v[126:129], 0
	v_add_f32_e32 v255, v59, v255
	v_cvt_pk_bf16_f32 v53, v56, v57
	v_add_f32_e32 v254, v60, v254
	v_cndmask_b32_e64 v132, 0, v53, s[92:93]
	v_cvt_pk_bf16_f32 v53, v58, v59
	v_add_f32_e32 v255, v61, v255
	v_cndmask_b32_e64 v133, 0, v53, s[92:93]
	ds_read_b64_tr_b16 v[166:167], v192 offset:25600
	ds_read_b64_tr_b16 v[168:169], v192 offset:26112
	s_waitcnt lgkmcnt(11)
	v_mfma_f32_32x32x16_bf16 v[68:83], v[158:161], v[122:125], v[68:83]
	v_add_f32_e32 v254, v62, v254
	v_add_f32_e32 v255, v63, v255
	v_cvt_pk_bf16_f32 v53, v60, v61
	v_add_f32_e32 v254, v64, v254
	v_cndmask_b32_e64 v108, 0, v53, s[92:93]
	v_cvt_pk_bf16_f32 v53, v62, v63
	v_add_f32_e32 v255, v65, v255
	v_cndmask_b32_e64 v109, 0, v53, s[92:93]
	ds_read_b64_tr_b16 v[170:171], v192 offset:29696
	ds_read_b64_tr_b16 v[172:173], v192 offset:30208
	s_waitcnt lgkmcnt(12)
	v_mfma_f32_32x32x16_bf16 v[84:99], v[150:153], v[122:125], v[84:99]
	v_add_f32_e32 v254, v66, v254
	v_add_f32_e32 v255, v67, v255
	v_cvt_pk_bf16_f32 v53, v64, v65
	v_add_f32_e32 v254, v36, v254
	v_cndmask_b32_e64 v110, 0, v53, s[92:93]
	v_cvt_pk_bf16_f32 v53, v66, v67
	v_add_f32_e32 v255, v37, v255
	v_cndmask_b32_e64 v111, 0, v53, s[92:93]
	ds_read_b64_tr_b16 v[174:175], v192 offset:26624
	ds_read_b64_tr_b16 v[176:177], v192 offset:27136
	s_waitcnt lgkmcnt(13)
	v_mfma_f32_32x32x16_bf16 v[68:83], v[146:149], v[118:121], v[68:83]
	v_add_f32_e32 v254, v38, v254
	v_add_f32_e32 v255, v39, v255
	v_cvt_pk_bf16_f32 v36, v36, v37
	v_add_f32_e32 v254, v40, v254
	v_cndmask_b32_e64 v104, 0, v36, s[92:93]
	v_cvt_pk_bf16_f32 v36, v38, v39
	v_add_f32_e32 v255, v41, v255
	v_cndmask_b32_e64 v105, 0, v36, s[92:93]
	ds_read_b64_tr_b16 v[178:179], v192 offset:30720
	ds_read_b64_tr_b16 v[180:181], v192 offset:31232
	s_waitcnt lgkmcnt(14)
	v_mfma_f32_32x32x16_bf16 v[84:99], v[142:145], v[118:121], v[84:99]
	v_add_f32_e32 v254, v42, v254
	v_add_f32_e32 v255, v43, v255
	v_cvt_pk_bf16_f32 v37, v40, v41
	v_add_f32_e32 v254, v44, v254
	v_cndmask_b32_e64 v106, 0, v37, s[92:93]
	v_cvt_pk_bf16_f32 v37, v42, v43
	v_add_f32_e32 v255, v45, v255
	v_cndmask_b32_e64 v107, 0, v37, s[92:93]
	ds_read_b64_tr_b16 v[186:187], v192 offset:27648
	ds_read_b64_tr_b16 v[188:189], v192 offset:28160
	s_waitcnt lgkmcnt(14)
	v_mfma_f32_32x32x16_bf16 v[68:83], v[138:141], v[114:117], v[68:83]
	v_add_f32_e32 v254, v46, v254
	v_add_f32_e32 v255, v47, v255
	v_cvt_pk_bf16_f32 v37, v44, v45
	v_add_f32_e32 v254, v48, v254
	v_cndmask_b32_e64 v100, 0, v37, s[92:93]
	v_cvt_pk_bf16_f32 v37, v46, v47
	v_add_f32_e32 v255, v49, v255
	v_cndmask_b32_e64 v101, 0, v37, s[92:93]
	ds_read_b64_tr_b16 v[190:191], v192 offset:31744
	ds_read_b64_tr_b16 v[192:193], v192 offset:32256
	v_mfma_f32_32x32x16_bf16 v[84:99], v[134:137], v[114:117], v[84:99]
	v_add_f32_e32 v254, v50, v254
	v_add_f32_e32 v255, v51, v255
	v_add_f32_e32 v36, v254, v255
	v_add_f32_e32 v134, 0, v36
	v_cvt_pk_bf16_f32 v36, v48, v49
	v_cndmask_b32_e64 v102, 0, v36, s[92:93]
	v_cvt_pk_bf16_f32 v36, v50, v51
	v_cndmask_b32_e64 v103, 0, v36, s[92:93]
	s_add_i32 s72, s76, 1
	s_cmp_ge_u32 s72, s83
	s_cselect_b64 s[80:81], -1, 0
	s_and_b64 vcc, exec, s[80:81]
	s_cbranch_vccnz .LBB0_1453
	v_mov_b32_e32 v36, s5
	ds_read_b32 v36, v36 offset:12
	s_waitcnt lgkmcnt(0)
	v_readfirstlane_b32 s72, v36
	s_lshl_b32 s72, s72, 13
	s_and_b32 s72, s72, 0x7e000
	s_add_u32 s72, s77, s72
	s_addc_u32 s73, s78, 0
	s_add_i32 s85, s84, s95
	s_mov_b32 s86, m0
	s_mov_b32 m0, s85
	s_nop 0
	global_load_lds_dwordx4 v236, s[72:73]
	s_mov_b32 m0, s86

.LBB0_1462:
	v_add_u32_e32 v176, s84, v239
	ds_read_b64_tr_b16 v[190:191], v176 offset:24576
	ds_read_b64_tr_b16 v[192:193], v176 offset:25088
	v_add_f32_e32 v254, v52, v53
	v_add_f32_e32 v255, v54, v55
	v_add_f32_e32 v254, v56, v254
	v_add_f32_e32 v255, v57, v255
	s_waitcnt lgkmcnt(9)
	v_mfma_f32_32x32x16_bf16 v[68:83], v[162:165], v[126:129], 0
	v_cvt_pk_bf16_f32 v52, v52, v53
	v_cndmask_b32_e64 v130, 0, v52, s[72:73]
	v_cvt_pk_bf16_f32 v52, v54, v55
	v_cndmask_b32_e64 v131, 0, v52, s[72:73]
	ds_read_b64_tr_b16 v[194:195], v176 offset:28672
	ds_read_b64_tr_b16 v[196:197], v176 offset:29184
	v_add_f32_e32 v254, v58, v254
	s_waitcnt lgkmcnt(10)
	v_mfma_f32_32x32x16_bf16 v[84:99], v[154:157], v[126:129], 0
	v_add_f32_e32 v255, v59, v255
	v_cvt_pk_bf16_f32 v53, v56, v57
	v_add_f32_e32 v254, v60, v254
	v_cndmask_b32_e64 v132, 0, v53, s[72:73]
	v_cvt_pk_bf16_f32 v53, v58, v59
	v_add_f32_e32 v255, v61, v255
	v_cndmask_b32_e64 v133, 0, v53, s[72:73]
	ds_read_b64_tr_b16 v[186:187], v176 offset:25600
	ds_read_b64_tr_b16 v[188:189], v176 offset:26112
	s_waitcnt lgkmcnt(11)
	v_mfma_f32_32x32x16_bf16 v[68:83], v[158:161], v[122:125], v[68:83]
	v_add_f32_e32 v254, v62, v254
	v_add_f32_e32 v255, v63, v255
	v_cvt_pk_bf16_f32 v53, v60, v61
	v_add_f32_e32 v254, v64, v254
	v_cndmask_b32_e64 v108, 0, v53, s[72:73]
	v_cvt_pk_bf16_f32 v53, v62, v63
	v_add_f32_e32 v255, v65, v255
	v_cndmask_b32_e64 v109, 0, v53, s[72:73]
	ds_read_b64_tr_b16 v[182:183], v176 offset:29696
	ds_read_b64_tr_b16 v[184:185], v176 offset:30208
	s_waitcnt lgkmcnt(12)
	v_mfma_f32_32x32x16_bf16 v[84:99], v[150:153], v[122:125], v[84:99]
	v_add_f32_e32 v254, v66, v254
	v_add_f32_e32 v255, v67, v255
	v_cvt_pk_bf16_f32 v53, v64, v65
	v_add_f32_e32 v254, v36, v254
	v_cndmask_b32_e64 v110, 0, v53, s[72:73]
	v_cvt_pk_bf16_f32 v53, v66, v67
	v_add_f32_e32 v255, v37, v255
	v_cndmask_b32_e64 v111, 0, v53, s[72:73]
	ds_read_b64_tr_b16 v[178:179], v176 offset:26624
	ds_read_b64_tr_b16 v[180:181], v176 offset:27136
	s_waitcnt lgkmcnt(13)
	v_mfma_f32_32x32x16_bf16 v[68:83], v[146:149], v[118:121], v[68:83]
	v_add_f32_e32 v254, v38, v254
	v_add_f32_e32 v255, v39, v255
	v_cvt_pk_bf16_f32 v36, v36, v37
	v_add_f32_e32 v254, v40, v254
	v_cndmask_b32_e64 v104, 0, v36, s[72:73]
	v_cvt_pk_bf16_f32 v36, v38, v39
	v_add_f32_e32 v255, v41, v255
	v_cndmask_b32_e64 v105, 0, v36, s[72:73]
	ds_read_b64_tr_b16 v[166:167], v176 offset:30720
	ds_read_b64_tr_b16 v[168:169], v176 offset:31232
	s_waitcnt lgkmcnt(14)
	v_mfma_f32_32x32x16_bf16 v[84:99], v[142:145], v[118:121], v[84:99]
	v_add_f32_e32 v254, v42, v254
	v_add_f32_e32 v255, v43, v255
	v_cvt_pk_bf16_f32 v37, v40, v41
	v_add_f32_e32 v254, v44, v254
	v_cndmask_b32_e64 v106, 0, v37, s[72:73]
	v_cvt_pk_bf16_f32 v37, v42, v43
	v_add_f32_e32 v255, v45, v255
	v_cndmask_b32_e64 v107, 0, v37, s[72:73]
	ds_read_b64_tr_b16 v[170:171], v176 offset:27648
	ds_read_b64_tr_b16 v[172:173], v176 offset:28160
	s_waitcnt lgkmcnt(14)
	v_mfma_f32_32x32x16_bf16 v[68:83], v[138:141], v[114:117], v[68:83]
	v_add_f32_e32 v254, v46, v254
	v_add_f32_e32 v255, v47, v255
	v_cvt_pk_bf16_f32 v37, v44, v45
	v_add_f32_e32 v254, v48, v254
	v_cndmask_b32_e64 v100, 0, v37, s[72:73]
	v_cvt_pk_bf16_f32 v37, v46, v47
	v_add_f32_e32 v255, v49, v255
	v_cndmask_b32_e64 v101, 0, v37, s[72:73]
	ds_read_b64_tr_b16 v[174:175], v176 offset:31744
	ds_read_b64_tr_b16 v[176:177], v176 offset:32256
	v_mfma_f32_32x32x16_bf16 v[84:99], v[134:137], v[114:117], v[84:99]
	v_add_f32_e32 v254, v50, v254
	v_add_f32_e32 v255, v51, v255
	v_add_f32_e32 v36, v254, v255
	v_add_f32_e32 v243, 0, v36
	v_cvt_pk_bf16_f32 v36, v48, v49
	v_cndmask_b32_e64 v102, 0, v36, s[72:73]
	v_cvt_pk_bf16_f32 v36, v50, v51
	v_cndmask_b32_e64 v103, 0, v36, s[72:73]
	s_add_i32 s85, s76, 2
	s_cmp_ge_u32 s85, s83
	s_cselect_b64 s[90:91], -1, 0
	s_and_b64 vcc, exec, s[90:91]
	s_cbranch_vccnz .LBB0_1464
	v_mov_b32_e32 v36, s5
	ds_read_b32 v36, v36 offset:16
	s_waitcnt lgkmcnt(0)
	v_readfirstlane_b32 s84, v36
	s_lshl_b32 s84, s84, 13
	s_and_b32 s84, s84, 0x7e000
	s_add_u32 s86, s77, s84
	s_addc_u32 s87, s78, 0
	s_add_i32 s84, s4, s95
	s_mov_b32 s92, m0
	s_mov_b32 m0, s84
	s_nop 0
	global_load_lds_dwordx4 v236, s[86:87]
	s_mov_b32 m0, s92

.LBB0_1504:
	v_add_u32_e32 v170, s4, v239
	ds_read_b64_tr_b16 v[166:167], v170 offset:24576
	ds_read_b64_tr_b16 v[168:169], v170 offset:25088
	v_add_f32_e32 v254, v52, v53
	v_add_f32_e32 v255, v54, v55
	v_cvt_pk_bf16_f32 v52, v52, v53
	v_add_f32_e32 v254, v56, v254
	v_cndmask_b32_e64 v130, 0, v52, s[92:93]
	v_cvt_pk_bf16_f32 v52, v54, v55
	v_add_f32_e32 v255, v57, v255
	v_cndmask_b32_e64 v131, 0, v52, s[92:93]
	s_waitcnt lgkmcnt(3)
	v_mfma_f32_32x32x16_bf16 v[68:83], v[162:165], v[126:129], 0
	ds_read_b64_tr_b16 v[162:163], v170 offset:28672
	ds_read_b64_tr_b16 v[164:165], v170 offset:29184
	v_add_f32_e32 v254, v58, v254
	v_add_f32_e32 v255, v59, v255
	v_cvt_pk_bf16_f32 v53, v56, v57
	v_add_f32_e32 v254, v60, v254
	v_cndmask_b32_e64 v132, 0, v53, s[92:93]
	v_cvt_pk_bf16_f32 v53, v58, v59
	v_add_f32_e32 v255, v61, v255
	v_cndmask_b32_e64 v133, 0, v53, s[92:93]
	s_waitcnt lgkmcnt(4)
	v_mfma_f32_32x32x16_bf16 v[84:99], v[154:157], v[126:129], 0
	ds_read_b64_tr_b16 v[154:155], v170 offset:25600
	ds_read_b64_tr_b16 v[156:157], v170 offset:26112
	v_add_f32_e32 v254, v62, v254
	v_add_f32_e32 v255, v63, v255
	v_cvt_pk_bf16_f32 v53, v60, v61
	v_add_f32_e32 v254, v64, v254
	v_cndmask_b32_e64 v108, 0, v53, s[92:93]
	v_cvt_pk_bf16_f32 v53, v62, v63
	v_add_f32_e32 v255, v65, v255
	v_cndmask_b32_e64 v109, 0, v53, s[92:93]
	v_mfma_f32_32x32x16_bf16 v[68:83], v[158:161], v[122:125], v[68:83]
	ds_read_b64_tr_b16 v[158:159], v170 offset:29696
	ds_read_b64_tr_b16 v[160:161], v170 offset:30208
	v_add_f32_e32 v254, v66, v254
	v_add_f32_e32 v255, v67, v255
	v_cvt_pk_bf16_f32 v53, v64, v65
	v_add_f32_e32 v254, v36, v254
	v_cndmask_b32_e64 v110, 0, v53, s[92:93]
	v_cvt_pk_bf16_f32 v53, v66, v67
	v_add_f32_e32 v255, v37, v255
	v_cndmask_b32_e64 v111, 0, v53, s[92:93]
	v_mfma_f32_32x32x16_bf16 v[84:99], v[150:153], v[122:125], v[84:99]
	ds_read_b64_tr_b16 v[150:151], v170 offset:26624
	ds_read_b64_tr_b16 v[152:153], v170 offset:27136
	v_add_f32_e32 v254, v38, v254
	v_add_f32_e32 v255, v39, v255
	v_cvt_pk_bf16_f32 v36, v36, v37
	v_add_f32_e32 v254, v40, v254
	v_cndmask_b32_e64 v104, 0, v36, s[92:93]
	v_cvt_pk_bf16_f32 v36, v38, v39
	v_add_f32_e32 v255, v41, v255
	v_cndmask_b32_e64 v105, 0, v36, s[92:93]
	v_mfma_f32_32x32x16_bf16 v[68:83], v[146:149], v[118:121], v[68:83]
	ds_read_b64_tr_b16 v[146:147], v170 offset:30720
	ds_read_b64_tr_b16 v[148:149], v170 offset:31232
	v_add_f32_e32 v254, v42, v254
	v_add_f32_e32 v255, v43, v255
	v_cvt_pk_bf16_f32 v37, v40, v41
	v_add_f32_e32 v254, v44, v254
	v_cndmask_b32_e64 v106, 0, v37, s[92:93]
	v_cvt_pk_bf16_f32 v37, v42, v43
	v_add_f32_e32 v255, v45, v255
	v_cndmask_b32_e64 v107, 0, v37, s[92:93]
	v_mfma_f32_32x32x16_bf16 v[84:99], v[142:145], v[118:121], v[84:99]
	ds_read_b64_tr_b16 v[142:143], v170 offset:27648
	ds_read_b64_tr_b16 v[144:145], v170 offset:28160
	v_add_f32_e32 v254, v46, v254
	v_add_f32_e32 v255, v47, v255
	v_cvt_pk_bf16_f32 v37, v44, v45
	v_add_f32_e32 v254, v48, v254
	v_cndmask_b32_e64 v100, 0, v37, s[92:93]
	v_cvt_pk_bf16_f32 v37, v46, v47
	v_add_f32_e32 v255, v49, v255
	v_cndmask_b32_e64 v101, 0, v37, s[92:93]
	v_mfma_f32_32x32x16_bf16 v[68:83], v[138:141], v[114:117], v[68:83]
	ds_read_b64_tr_b16 v[138:139], v170 offset:31744
	ds_read_b64_tr_b16 v[140:141], v170 offset:32256
	v_add_f32_e32 v254, v50, v254
	v_add_f32_e32 v255, v51, v255
	v_add_f32_e32 v36, v254, v255
	v_mfma_f32_32x32x16_bf16 v[84:99], v[134:137], v[114:117], v[84:99]
	v_add_f32_e32 v134, 0, v36
	v_cvt_pk_bf16_f32 v36, v48, v49
	v_cndmask_b32_e64 v102, 0, v36, s[92:93]
	v_cvt_pk_bf16_f32 v36, v50, v51
	v_cndmask_b32_e64 v103, 0, v36, s[92:93]
	s_lshl_b32 s4, s83, 2
	s_add_i32 s4, s4, 0
	s_add_i32 s4, s4, 0x1d9fc
	v_mov_b32_e32 v36, s4
	ds_read_b32 v36, v36
	v_pk_add_f32 v[52:53], v[68:69], v[2:3] op_sel_hi:[1,0] neg_lo:[0,1] neg_hi:[0,1]
	v_pk_add_f32 v[54:55], v[70:71], v[2:3] op_sel_hi:[1,0] neg_lo:[0,1] neg_hi:[0,1]
	v_pk_add_f32 v[38:39], v[86:87], v[2:3] op_sel_hi:[1,0] neg_lo:[0,1] neg_hi:[0,1]
	v_pk_add_f32 v[56:57], v[72:73], v[2:3] op_sel_hi:[1,0] neg_lo:[0,1] neg_hi:[0,1]
	s_waitcnt lgkmcnt(0)
	v_readfirstlane_b32 s4, v36
	s_and_b32 s5, s4, 63
	s_sub_i32 s6, s94, s5
	v_pk_add_f32 v[36:37], v[84:85], v[2:3] op_sel_hi:[1,0] neg_lo:[0,1] neg_hi:[0,1]
	v_pk_add_f32 v[40:41], v[88:89], v[2:3] op_sel_hi:[1,0] neg_lo:[0,1] neg_hi:[0,1]
	v_pk_add_f32 v[58:59], v[74:75], v[2:3] op_sel_hi:[1,0] neg_lo:[0,1] neg_hi:[0,1]
	v_pk_add_f32 v[42:43], v[90:91], v[2:3] op_sel_hi:[1,0] neg_lo:[0,1] neg_hi:[0,1]
	v_pk_add_f32 v[60:61], v[76:77], v[2:3] op_sel_hi:[1,0] neg_lo:[0,1] neg_hi:[0,1]
	v_pk_add_f32 v[44:45], v[92:93], v[2:3] op_sel_hi:[1,0] neg_lo:[0,1] neg_hi:[0,1]
	v_pk_add_f32 v[62:63], v[78:79], v[2:3] op_sel_hi:[1,0] neg_lo:[0,1] neg_hi:[0,1]
	v_pk_add_f32 v[46:47], v[94:95], v[2:3] op_sel_hi:[1,0] neg_lo:[0,1] neg_hi:[0,1]
	v_pk_add_f32 v[64:65], v[80:81], v[2:3] op_sel_hi:[1,0] neg_lo:[0,1] neg_hi:[0,1]
	v_pk_add_f32 v[48:49], v[96:97], v[2:3] op_sel_hi:[1,0] neg_lo:[0,1] neg_hi:[0,1]
	v_pk_add_f32 v[66:67], v[82:83], v[2:3] op_sel_hi:[1,0] neg_lo:[0,1] neg_hi:[0,1]
	v_pk_add_f32 v[50:51], v[98:99], v[2:3] op_sel_hi:[1,0] neg_lo:[0,1] neg_hi:[0,1]
	s_cmp_gt_i32 s6, 2
	s_cbranch_scc1 .LBB0_1506
	s_lshl_b32 s6, s6, 8
	v_sub_u32_e32 v2, v234, v233
	s_add_i32 s6, s6, s33
	v_lshl_add_u32 v2, v2, 2, s6
	ds_read_b32 v68, v2 offset:256
	ds_read_b32 v70, v2 offset:128
	ds_read_b32 v69, v2 offset:252
	ds_read_b32 v71, v2 offset:124
	ds_read_b32 v72, v2 offset:248
	ds_read_b32 v74, v2 offset:120
	ds_read_b32 v73, v2 offset:244
	ds_read_b32 v75, v2 offset:116
	ds_read_b32 v76, v2 offset:224
	ds_read_b32 v78, v2 offset:96
	ds_read_b32 v77, v2 offset:220
	ds_read_b32 v79, v2 offset:92
	ds_read_b32 v80, v2 offset:216
	ds_read_b32 v82, v2 offset:88
	ds_read_b32 v81, v2 offset:212
	ds_read_b32 v83, v2 offset:84
	ds_read_b32 v84, v2 offset:192
	ds_read_b32 v86, v2 offset:64
	ds_read_b32 v85, v2 offset:188
	ds_read_b32 v87, v2 offset:60
	ds_read_b32 v88, v2 offset:184
	ds_read_b32 v90, v2 offset:56
	ds_read_b32 v89, v2 offset:180
	ds_read_b32 v91, v2 offset:52
	ds_read_b32 v92, v2 offset:160
	ds_read_b32 v94, v2 offset:32
	ds_read_b32 v93, v2 offset:156
	ds_read_b32 v95, v2 offset:28
	ds_read_b32 v96, v2 offset:152
	ds_read_b32 v98, v2 offset:24
	ds_read_b32 v97, v2 offset:148
	ds_read_b32 v99, v2 offset:20
	s_waitcnt lgkmcnt(14)
	v_pk_add_f32 v[52:53], v[52:53], v[68:69]
	v_pk_add_f32 v[54:55], v[54:55], v[72:73]
	v_pk_add_f32 v[56:57], v[56:57], v[76:77]
	v_pk_add_f32 v[58:59], v[58:59], v[80:81]
	s_waitcnt lgkmcnt(13)
	v_pk_add_f32 v[60:61], v[60:61], v[84:85]
	s_waitcnt lgkmcnt(9)
	v_pk_add_f32 v[62:63], v[62:63], v[88:89]
	s_waitcnt lgkmcnt(5)
	v_pk_add_f32 v[64:65], v[64:65], v[92:93]
	s_waitcnt lgkmcnt(1)
	v_pk_add_f32 v[66:67], v[66:67], v[96:97]
	v_pk_add_f32 v[36:37], v[36:37], v[70:71]
	v_pk_add_f32 v[38:39], v[38:39], v[74:75]
	v_pk_add_f32 v[40:41], v[40:41], v[78:79]
	v_pk_add_f32 v[42:43], v[42:43], v[82:83]
	v_pk_add_f32 v[44:45], v[44:45], v[86:87]
	v_pk_add_f32 v[46:47], v[46:47], v[90:91]
	v_pk_add_f32 v[48:49], v[48:49], v[94:95]
	s_waitcnt lgkmcnt(0)
	v_pk_add_f32 v[50:51], v[50:51], v[98:99]

; #define SBAR() __builtin_amdgcn_sched_barrier(0)
;   #define PKW(P,B) cvtpk_s(P[B],P[B+1])
;   #define PKW(P,B) cvtpk_s(P[B],P[B+1])
; template<bool WIN,int THRL> __device__ __forceinline__ void nsa_branch_pipe(const bf16*__restrict__ Kb,const bf16*__restrict__ Vb,const __attribute__((address_space(3))) int*tl,int NT,int qc,const bf16x8*qr,unsigned selbits, ...
;     ...
;   { float sacc=pB0[0]+pB0[1]; _Pragma("unroll") for(int r=2;r<16;++r)sacc+=pB0[r]; _Pragma("unroll") for(int r=0;r<16;++r)sacc+=pB1[r]; l_reg+=(amB?sacc:0.f);
;     pw0=(u32x4){PKW(pB0,0)&amB,PKW(pB0,2)&amB,PKW(pB0,4)&amB,PKW(pB0,6)&amB};pw1=(u32x4){PKW(pB0,8)&amB,PKW(pB0,10)&amB,PKW(pB0,12)&amB,PKW(pB0,14)&amB};pw2=(u32x4){PKW(pB1,0)&amB,PKW(pB1,2)&amB,PKW(pB1,4)&amB,PKW(pB1,6)&amB};pw3=(u32x4){PKW(pB1,8)&amB,PKW(pB1,10)&amB,PKW(pB1,12)&amB,PKW(pB1,14)&amB};
;     SBAR(); pv(o,vb0+sl_cur,PAF(0),PAF(1),PAF(2),PAF(3)); }
;     ...
;   {auto rr=__builtin_amdgcn_permlane32_swap(__float_as_uint(l_reg),__float_as_uint(l_reg),false,false);l_out=__uint_as_float(rr[0])+__uint_as_float(rr[1]);}
; __device__ __forceinline__ void nsa_unit(int b, int g, int qc, const bf16* Q, const bf16* KV, const bf16* KC2, size_t kvstride, size_t kc2stride, const float* gates, const float* lutg, bf16* O, char* shm) {
;     ...
;       nsa_branch_pipe<false, 32>(kvb + 2 * kvstride, kvb + 3 * kvstride, (const __attribute__((address_space(3))) int*)(shm3 + L_TL), NTs, qc, qr, selm, luth, shm, lt, ob);
;       const float gs = gl[64 + lane]; stash_acc(stash, ob, lt > 0.f ? gs * __builtin_amdgcn_rcpf(lt) : 0.f, wsf, lane, r32, hi, false); }
.LBB0_1511:
	v_add_f32_e32 v254, v52, v53
	v_add_f32_e32 v255, v54, v55
	v_add_f32_e32 v254, v56, v254
	v_add_f32_e32 v255, v57, v255
	v_add_f32_e32 v254, v58, v254
	v_add_f32_e32 v255, v59, v255
	v_add_f32_e32 v254, v60, v254
	v_add_f32_e32 v255, v61, v255
	v_add_f32_e32 v254, v62, v254
	v_add_f32_e32 v255, v63, v255
	v_add_f32_e32 v254, v64, v254
	v_add_f32_e32 v255, v65, v255
	v_add_f32_e32 v254, v66, v254
	v_add_f32_e32 v255, v67, v255
	v_add_f32_e32 v254, v36, v254
	v_add_f32_e32 v255, v37, v255
	v_add_f32_e32 v254, v38, v254
	v_add_f32_e32 v255, v39, v255
	v_add_f32_e32 v254, v40, v254
	v_add_f32_e32 v255, v41, v255
	v_add_f32_e32 v254, v42, v254
	v_add_f32_e32 v255, v43, v255
	v_add_f32_e32 v254, v44, v254
	v_add_f32_e32 v255, v45, v255
	v_add_f32_e32 v254, v46, v254
	v_add_f32_e32 v255, v47, v255
	v_add_f32_e32 v254, v48, v254
	v_add_f32_e32 v255, v49, v255
	v_add_f32_e32 v254, v50, v254
	v_add_f32_e32 v255, v51, v255
	v_add_f32_e32 v68, v254, v255
	s_cmp_lg_u32 0, -1
	s_cselect_b32 s6, 0, 0
	v_cndmask_b32_e64 v68, 0, v68, s[4:5]
	v_cvt_pk_bf16_f32 v36, v36, v37
	s_addk_i32 s6, 0x6000
	v_add_f32_e32 v2, v2, v68
	v_cvt_pk_bf16_f32 v52, v52, v53
	v_cvt_pk_bf16_f32 v53, v54, v55
	v_cvt_pk_bf16_f32 v54, v56, v57
	v_cvt_pk_bf16_f32 v55, v58, v59
	v_cvt_pk_bf16_f32 v56, v60, v61
	v_cvt_pk_bf16_f32 v57, v62, v63
	v_cvt_pk_bf16_f32 v58, v64, v65
	v_cvt_pk_bf16_f32 v59, v66, v67
	v_cndmask_b32_e64 v36, 0, v36, s[4:5]
	v_cvt_pk_bf16_f32 v37, v38, v39
	v_cvt_pk_bf16_f32 v38, v40, v41
	v_cvt_pk_bf16_f32 v39, v42, v43
	v_cvt_pk_bf16_f32 v40, v44, v45
	v_cvt_pk_bf16_f32 v41, v46, v47
	v_cvt_pk_bf16_f32 v42, v48, v49
	v_cvt_pk_bf16_f32 v43, v50, v51
	v_add3_u32 v69, v231, s6, v112
	v_cndmask_b32_e64 v52, 0, v52, s[4:5]
	v_cndmask_b32_e64 v53, 0, v53, s[4:5]
	v_cndmask_b32_e64 v54, 0, v54, s[4:5]
	v_cndmask_b32_e64 v55, 0, v55, s[4:5]
	v_cndmask_b32_e64 v56, 0, v56, s[4:5]
	v_cndmask_b32_e64 v57, 0, v57, s[4:5]
	v_cndmask_b32_e64 v58, 0, v58, s[4:5]
	v_cndmask_b32_e64 v59, 0, v59, s[4:5]
	v_cndmask_b32_e64 v37, 0, v37, s[4:5]
	v_cndmask_b32_e64 v38, 0, v38, s[4:5]
	v_cndmask_b32_e64 v39, 0, v39, s[4:5]
	v_cndmask_b32_e64 v40, 0, v40, s[4:5]
	v_cndmask_b32_e64 v41, 0, v41, s[4:5]
	v_cndmask_b32_e64 v42, 0, v42, s[4:5]
	v_cndmask_b32_e64 v43, 0, v43, s[4:5]
	v_add3_u32 v68, v69, v210, s84
	ds_read_b64_tr_b16 v[44:45],v68 offset:0
	ds_read_b64_tr_b16 v[46:47],v68 offset:512
	ds_read_b64_tr_b16 v[48:49],v68 offset:1024
	ds_read_b64_tr_b16 v[50:51],v68 offset:1536
	ds_read_b64_tr_b16 v[60:61],v68 offset:2048
	ds_read_b64_tr_b16 v[62:63],v68 offset:2560
	ds_read_b64_tr_b16 v[64:65],v68 offset:3072
	ds_read_b64_tr_b16 v[66:67],v68 offset:3584
	s_waitcnt lgkmcnt(0)
	s_nop 0
	v_mfma_f32_32x32x16_bf16 v[20:35], v[52:55], v[44:47], v[20:35]
	ds_read_b64_tr_b16 v[44:45],v68 offset:4096
	ds_read_b64_tr_b16 v[46:47],v68 offset:4608
	v_mfma_f32_32x32x16_bf16 v[20:35], v[56:59], v[48:51], v[20:35]
	ds_read_b64_tr_b16 v[48:49],v68 offset:5120
	ds_read_b64_tr_b16 v[50:51],v68 offset:5632
	v_mfma_f32_32x32x16_bf16 v[20:35], v[36:39], v[60:63], v[20:35]
	ds_read_b64_tr_b16 v[60:61],v68 offset:6144
	ds_read_b64_tr_b16 v[62:63],v68 offset:6656
	v_mfma_f32_32x32x16_bf16 v[20:35], v[40:43], v[64:67], v[20:35]
	ds_read_b64_tr_b16 v[64:65],v68 offset:7168
	ds_read_b64_tr_b16 v[66:67],v68 offset:7680
	s_waitcnt lgkmcnt(0)
	v_mfma_f32_32x32x16_bf16 v[4:19], v[52:55], v[44:47], v[4:19]
	s_waitcnt lgkmcnt(0)
	s_barrier
	v_mfma_f32_32x32x16_bf16 v[4:19], v[56:59], v[48:51], v[4:19]
	v_mfma_f32_32x32x16_bf16 v[4:19], v[36:39], v[60:63], v[4:19]
	v_mov_b32_e32 v36, v2
	s_nop 1
	v_permlane32_swap_b32_e32 v2, v36
	v_mfma_f32_32x32x16_bf16 v[4:19], v[40:43], v[64:67], v[4:19]
	s_and_saveexec_b64 s[4:5], s[2:3]
	s_cbranch_execz .LBB0_1513
	v_add_f32_e32 v2, v2, v36
	ds_read_b32 v36, v227 offset:256
	v_cmp_lt_f32_e32 vcc, 0, v2
	v_rcp_f32_e32 v2, v2
	v_readlane_b32 s6, v252, 33
	s_waitcnt lgkmcnt(0)
	v_mul_f32_e32 v2, v2, v36
	v_lshl_add_u32 v37, v212, 2, s6
	v_cndmask_b32_e32 v2, 0, v2, vcc
	ds_write_b32 v37, v2 offset:49152

.LBB0_1519:
	v_add_u32_e32 v2, s72, v241
	ds_read_b64_tr_b16 v[8:9], v2 offset:24576
	ds_read_b64_tr_b16 v[10:11], v2 offset:25088
	v_add_f32_e32 v254, v66, v67
	v_add_f32_e32 v255, v68, v69
	v_cvt_pk_bf16_f32 v5, v66, v67
	v_add_f32_e32 v254, v70, v254
	v_cndmask_b32_e64 v142, 0, v5, s[92:93]
	v_cvt_pk_bf16_f32 v5, v68, v69
	v_add_f32_e32 v255, v71, v255
	v_cndmask_b32_e64 v143, 0, v5, s[92:93]
	s_waitcnt lgkmcnt(9)
	v_mfma_f32_32x32x16_bf16 v[82:97], v[174:177], v[126:129], 0
	ds_read_b64_tr_b16 v[12:13], v2 offset:28672
	ds_read_b64_tr_b16 v[14:15], v2 offset:29184
	v_add_f32_e32 v254, v72, v254
	v_add_f32_e32 v255, v73, v255
	v_add_f32_e32 v254, v74, v254
	v_add_f32_e32 v255, v75, v255
	v_cvt_pk_bf16_f32 v4, v70, v71
	v_cndmask_b32_e64 v144, 0, v4, s[92:93]
	v_cvt_pk_bf16_f32 v4, v72, v73
	v_cndmask_b32_e64 v145, 0, v4, s[92:93]
	s_waitcnt lgkmcnt(10)
	v_mfma_f32_32x32x16_bf16 v[98:113], v[166:169], v[126:129], 0
	ds_read_b64_tr_b16 v[4:5], v2 offset:25600
	ds_read_b64_tr_b16 v[6:7], v2 offset:26112
	v_add_f32_e32 v254, v76, v254
	v_add_f32_e32 v255, v77, v255
	v_cvt_pk_bf16_f32 v17, v74, v75
	v_add_f32_e32 v254, v78, v254
	v_cndmask_b32_e64 v138, 0, v17, s[92:93]
	v_cvt_pk_bf16_f32 v17, v76, v77
	v_add_f32_e32 v255, v79, v255
	v_cndmask_b32_e64 v139, 0, v17, s[92:93]
	s_waitcnt lgkmcnt(11)
	v_mfma_f32_32x32x16_bf16 v[82:97], v[170:173], v[122:125], v[82:97]
	ds_read_b64_tr_b16 v[166:167], v2 offset:29696
	ds_read_b64_tr_b16 v[168:169], v2 offset:30208
	v_add_f32_e32 v254, v80, v254
	v_add_f32_e32 v255, v81, v255
	v_cvt_pk_bf16_f32 v17, v78, v79
	v_add_f32_e32 v254, v50, v254
	v_cndmask_b32_e64 v140, 0, v17, s[92:93]
	v_cvt_pk_bf16_f32 v17, v80, v81
	v_add_f32_e32 v255, v51, v255
	v_cndmask_b32_e64 v141, 0, v17, s[92:93]
	s_waitcnt lgkmcnt(12)
	v_mfma_f32_32x32x16_bf16 v[98:113], v[162:165], v[122:125], v[98:113]
	ds_read_b64_tr_b16 v[162:163], v2 offset:26624
	ds_read_b64_tr_b16 v[164:165], v2 offset:27136
	v_add_f32_e32 v254, v52, v254
	v_add_f32_e32 v255, v53, v255
	v_cvt_pk_bf16_f32 v17, v50, v51
	v_add_f32_e32 v254, v54, v254
	v_cndmask_b32_e64 v134, 0, v17, s[92:93]
	v_cvt_pk_bf16_f32 v17, v52, v53
	v_add_f32_e32 v255, v55, v255
	v_cndmask_b32_e64 v135, 0, v17, s[92:93]
	s_waitcnt lgkmcnt(13)
	v_mfma_f32_32x32x16_bf16 v[82:97], v[158:161], v[118:121], v[82:97]
	ds_read_b64_tr_b16 v[158:159], v2 offset:30720
	ds_read_b64_tr_b16 v[160:161], v2 offset:31232
	v_add_f32_e32 v254, v56, v254
	v_add_f32_e32 v255, v57, v255
	v_cvt_pk_bf16_f32 v17, v54, v55
	v_add_f32_e32 v254, v58, v254
	v_cndmask_b32_e64 v136, 0, v17, s[92:93]
	v_cvt_pk_bf16_f32 v17, v56, v57
	v_add_f32_e32 v255, v59, v255
	v_cndmask_b32_e64 v137, 0, v17, s[92:93]
	s_waitcnt lgkmcnt(14)
	v_mfma_f32_32x32x16_bf16 v[98:113], v[154:157], v[118:121], v[98:113]
	ds_read_b64_tr_b16 v[154:155], v2 offset:27648
	ds_read_b64_tr_b16 v[156:157], v2 offset:28160
	v_add_f32_e32 v254, v60, v254
	v_add_f32_e32 v255, v61, v255
	v_cvt_pk_bf16_f32 v17, v58, v59
	v_add_f32_e32 v254, v62, v254
	v_cndmask_b32_e64 v130, 0, v17, s[92:93]
	v_cvt_pk_bf16_f32 v17, v60, v61
	v_add_f32_e32 v255, v63, v255
	v_cndmask_b32_e64 v131, 0, v17, s[92:93]
	s_waitcnt lgkmcnt(14)
	v_mfma_f32_32x32x16_bf16 v[82:97], v[150:153], v[114:117], v[82:97]
	ds_read_b64_tr_b16 v[150:151], v2 offset:31744
	ds_read_b64_tr_b16 v[152:153], v2 offset:32256
	v_add_f32_e32 v254, v64, v254
	v_cvt_pk_bf16_f32 v16, v62, v63
	v_add_f32_e32 v255, v65, v255
	v_add_f32_e32 v2, v254, v255
	v_cndmask_b32_e64 v132, 0, v16, s[92:93]
	v_cvt_pk_bf16_f32 v16, v64, v65
	v_add_f32_e32 v2, 0, v2
	v_cndmask_b32_e64 v133, 0, v16, s[92:93]
	v_mfma_f32_32x32x16_bf16 v[98:113], v[146:149], v[114:117], v[98:113]
	v_mov_b32_e32 v16, s85
	ds_read_b32 v17, v16 offset:12
	v_add_f32_e64 v66, v82, -v210
	v_add_f32_e64 v67, v83, -v210
	s_nop 7
	v_pk_add_f32 v[50:51], v[98:99], v[210:211] op_sel_hi:[1,0] neg_lo:[0,1] neg_hi:[0,1]
	v_pk_add_f32 v[68:69], v[84:85], v[210:211] op_sel_hi:[1,0] neg_lo:[0,1] neg_hi:[0,1]
	v_pk_add_f32 v[52:53], v[100:101], v[210:211] op_sel_hi:[1,0] neg_lo:[0,1] neg_hi:[0,1]
	s_waitcnt lgkmcnt(0)
	v_readfirstlane_b32 s4, v17
	s_lshl_b32 s4, s4, 13
	s_and_b32 s4, s4, 0x7e000
	s_add_u32 s72, s89, s4
	s_addc_u32 s73, s0, 0
	s_add_i32 s4, s91, s75
	s_mov_b32 s76, m0
	s_mov_b32 m0, s4
	s_nop 0
	global_load_lds_dwordx4 v238, s[72:73]
	s_mov_b32 m0, s76
	ds_read_b32 v17, v16 offset:4
	v_pk_add_f32 v[70:71], v[86:87], v[210:211] op_sel_hi:[1,0] neg_lo:[0,1] neg_hi:[0,1]
	v_pk_add_f32 v[54:55], v[102:103], v[210:211] op_sel_hi:[1,0] neg_lo:[0,1] neg_hi:[0,1]
	v_pk_add_f32 v[72:73], v[88:89], v[210:211] op_sel_hi:[1,0] neg_lo:[0,1] neg_hi:[0,1]
	v_pk_add_f32 v[56:57], v[104:105], v[210:211] op_sel_hi:[1,0] neg_lo:[0,1] neg_hi:[0,1]
	s_waitcnt lgkmcnt(0)
	v_readfirstlane_b32 s4, v17
	s_lshl_b32 s4, s4, 13
	s_and_b32 s4, s4, 0x7e000
	s_add_u32 s72, s1, s4
	s_addc_u32 s73, s74, 0
	s_add_i32 s4, s90, s95
	s_mov_b32 s76, m0
	s_mov_b32 m0, s4
	s_nop 0
	global_load_lds_dwordx4 v239, s[72:73]
	s_mov_b32 m0, s76
	ds_read_b32 v16, v16
	v_pk_add_f32 v[74:75], v[90:91], v[210:211] op_sel_hi:[1,0] neg_lo:[0,1] neg_hi:[0,1]
	v_pk_add_f32 v[58:59], v[106:107], v[210:211] op_sel_hi:[1,0] neg_lo:[0,1] neg_hi:[0,1]
	v_pk_add_f32 v[76:77], v[92:93], v[210:211] op_sel_hi:[1,0] neg_lo:[0,1] neg_hi:[0,1]
	v_pk_add_f32 v[60:61], v[108:109], v[210:211] op_sel_hi:[1,0] neg_lo:[0,1] neg_hi:[0,1]
	s_waitcnt lgkmcnt(0)
	v_readfirstlane_b32 s4, v16
	s_and_b32 s72, s4, 63
	s_sub_i32 s73, s94, s72
	v_pk_add_f32 v[78:79], v[94:95], v[210:211] op_sel_hi:[1,0] neg_lo:[0,1] neg_hi:[0,1]
	v_pk_add_f32 v[62:63], v[110:111], v[210:211] op_sel_hi:[1,0] neg_lo:[0,1] neg_hi:[0,1]
	v_pk_add_f32 v[80:81], v[96:97], v[210:211] op_sel_hi:[1,0] neg_lo:[0,1] neg_hi:[0,1]
	v_pk_add_f32 v[64:65], v[112:113], v[210:211] op_sel_hi:[1,0] neg_lo:[0,1] neg_hi:[0,1]
	s_cmp_gt_i32 s73, 2
	s_cbranch_scc0 .LBB0_1535
	s_cmp_lg_u32 s94, s72
	s_cbranch_scc0 .LBB0_1536

.LBB0_1526:
	s_add_i32 s4, s90, 0x2000
	s_cmpk_lg_i32 s90, 0x4000
	s_cselect_b32 s84, s4, 0
	v_add_u32_e32 v16, s91, v241
	ds_read_b64_tr_b16 v[8:9], v16 offset:24576
	ds_read_b64_tr_b16 v[10:11], v16 offset:25088
	v_add_f32_e32 v254, v66, v67
	v_add_f32_e32 v255, v68, v69
	v_cvt_pk_bf16_f32 v5, v66, v67
	v_add_f32_e32 v254, v70, v254
	v_cndmask_b32_e64 v142, 0, v5, s[72:73]
	v_cvt_pk_bf16_f32 v5, v68, v69
	v_add_f32_e32 v255, v71, v255
	v_cndmask_b32_e64 v143, 0, v5, s[72:73]
	s_waitcnt lgkmcnt(9)
	v_mfma_f32_32x32x16_bf16 v[82:97], v[12:15], v[126:129], 0
	ds_read_b64_tr_b16 v[12:13], v16 offset:28672
	ds_read_b64_tr_b16 v[14:15], v16 offset:29184
	v_add_f32_e32 v254, v72, v254
	v_add_f32_e32 v255, v73, v255
	v_add_f32_e32 v254, v74, v254
	v_add_f32_e32 v255, v75, v255
	v_cvt_pk_bf16_f32 v4, v70, v71
	v_cndmask_b32_e64 v144, 0, v4, s[72:73]
	v_cvt_pk_bf16_f32 v4, v72, v73
	v_cndmask_b32_e64 v145, 0, v4, s[72:73]
	s_waitcnt lgkmcnt(10)
	v_mfma_f32_32x32x16_bf16 v[98:113], v[98:101], v[126:129], 0
	ds_read_b64_tr_b16 v[4:5], v16 offset:25600
	ds_read_b64_tr_b16 v[6:7], v16 offset:26112
	v_add_f32_e32 v254, v76, v254
	v_add_f32_e32 v255, v77, v255
	v_cvt_pk_bf16_f32 v66, v74, v75
	v_add_f32_e32 v254, v78, v254
	v_cndmask_b32_e64 v138, 0, v66, s[72:73]
	v_cvt_pk_bf16_f32 v66, v76, v77
	v_add_f32_e32 v255, v79, v255
	v_cndmask_b32_e64 v139, 0, v66, s[72:73]
	s_waitcnt lgkmcnt(11)
	v_mfma_f32_32x32x16_bf16 v[82:97], v[146:149], v[122:125], v[82:97]
	ds_read_b64_tr_b16 v[146:147], v16 offset:29696
	ds_read_b64_tr_b16 v[148:149], v16 offset:30208
	v_add_f32_e32 v254, v80, v254
	v_add_f32_e32 v255, v81, v255
	v_cvt_pk_bf16_f32 v66, v78, v79
	v_add_f32_e32 v254, v50, v254
	v_cndmask_b32_e64 v140, 0, v66, s[72:73]
	v_cvt_pk_bf16_f32 v66, v80, v81
	v_add_f32_e32 v255, v51, v255
	v_cndmask_b32_e64 v141, 0, v66, s[72:73]
	s_waitcnt lgkmcnt(12)
	v_mfma_f32_32x32x16_bf16 v[98:113], v[178:181], v[122:125], v[98:113]
	ds_read_b64_tr_b16 v[150:151], v16 offset:26624
	ds_read_b64_tr_b16 v[152:153], v16 offset:27136
	v_add_f32_e32 v254, v52, v254
	v_add_f32_e32 v255, v53, v255
	v_cvt_pk_bf16_f32 v50, v50, v51
	v_add_f32_e32 v254, v54, v254
	v_cndmask_b32_e64 v134, 0, v50, s[72:73]
	v_cvt_pk_bf16_f32 v50, v52, v53
	v_add_f32_e32 v255, v55, v255
	v_cndmask_b32_e64 v135, 0, v50, s[72:73]
	s_waitcnt lgkmcnt(13)
	v_mfma_f32_32x32x16_bf16 v[82:97], v[174:177], v[118:121], v[82:97]
	ds_read_b64_tr_b16 v[178:179], v16 offset:30720
	ds_read_b64_tr_b16 v[180:181], v16 offset:31232
	v_add_f32_e32 v254, v56, v254
	v_add_f32_e32 v255, v57, v255
	v_cvt_pk_bf16_f32 v50, v54, v55
	v_add_f32_e32 v254, v58, v254
	v_cndmask_b32_e64 v136, 0, v50, s[72:73]
	v_cvt_pk_bf16_f32 v50, v56, v57
	v_add_f32_e32 v255, v59, v255
	v_cndmask_b32_e64 v137, 0, v50, s[72:73]
	s_waitcnt lgkmcnt(14)
	v_mfma_f32_32x32x16_bf16 v[98:113], v[170:173], v[118:121], v[98:113]
	ds_read_b64_tr_b16 v[182:183], v16 offset:27648
	ds_read_b64_tr_b16 v[184:185], v16 offset:28160
	v_add_f32_e32 v254, v60, v254
	v_add_f32_e32 v255, v61, v255
	v_cvt_pk_bf16_f32 v50, v58, v59
	v_add_f32_e32 v254, v62, v254
	v_cndmask_b32_e64 v130, 0, v50, s[72:73]
	v_cvt_pk_bf16_f32 v50, v60, v61
	v_add_f32_e32 v255, v63, v255
	v_cndmask_b32_e64 v131, 0, v50, s[72:73]
	s_waitcnt lgkmcnt(14)
	v_mfma_f32_32x32x16_bf16 v[82:97], v[166:169], v[114:117], v[82:97]
	ds_read_b64_tr_b16 v[186:187], v16 offset:31744
	ds_read_b64_tr_b16 v[188:189], v16 offset:32256
	v_add_f32_e32 v254, v64, v254
	v_cvt_pk_bf16_f32 v17, v62, v63
	v_add_f32_e32 v255, v65, v255
	v_add_f32_e32 v16, v254, v255
	v_cndmask_b32_e64 v132, 0, v17, s[72:73]
	v_cvt_pk_bf16_f32 v17, v64, v65
	v_add_f32_e32 v16, 0, v16
	v_cndmask_b32_e64 v133, 0, v17, s[72:73]
	v_mfma_f32_32x32x16_bf16 v[98:113], v[162:165], v[114:117], v[98:113]
	v_mov_b32_e32 v17, s85
	ds_read_b32 v50, v17 offset:16
	v_add_f32_e64 v66, v82, -v210
	v_add_f32_e64 v67, v83, -v210
	v_add_f32_e64 v68, v84, -v210
	v_add_f32_e64 v69, v85, -v210
	s_nop 5
	v_pk_add_f32 v[52:53], v[100:101], v[210:211] op_sel_hi:[1,0] neg_lo:[0,1] neg_hi:[0,1]
	v_pk_add_f32 v[70:71], v[86:87], v[210:211] op_sel_hi:[1,0] neg_lo:[0,1] neg_hi:[0,1]
	s_waitcnt lgkmcnt(0)
	v_readfirstlane_b32 s4, v50
	s_lshl_b32 s4, s4, 13
	s_and_b32 s4, s4, 0x7e000
	s_add_u32 s80, s89, s4
	s_addc_u32 s81, s0, 0
	s_add_i32 s4, s90, s75
	s_mov_b32 s76, m0
	s_mov_b32 m0, s4
	s_nop 0
	global_load_lds_dwordx4 v238, s[80:81]
	s_mov_b32 m0, s76
	ds_read_b32 v50, v17 offset:8
	v_pk_add_f32 v[54:55], v[102:103], v[210:211] op_sel_hi:[1,0] neg_lo:[0,1] neg_hi:[0,1]
	v_pk_add_f32 v[72:73], v[88:89], v[210:211] op_sel_hi:[1,0] neg_lo:[0,1] neg_hi:[0,1]
	v_pk_add_f32 v[56:57], v[104:105], v[210:211] op_sel_hi:[1,0] neg_lo:[0,1] neg_hi:[0,1]
	v_pk_add_f32 v[74:75], v[90:91], v[210:211] op_sel_hi:[1,0] neg_lo:[0,1] neg_hi:[0,1]
	s_waitcnt lgkmcnt(0)
	v_readfirstlane_b32 s4, v50
	s_lshl_b32 s4, s4, 13
	s_and_b32 s4, s4, 0x7e000
	s_add_u32 s80, s1, s4
	s_addc_u32 s81, s74, 0
	s_add_i32 s4, s84, s95
	s_mov_b32 s76, m0
	s_mov_b32 m0, s4
	s_nop 0
	global_load_lds_dwordx4 v239, s[80:81]
	s_mov_b32 m0, s76
	ds_read_b32 v17, v17 offset:4
	v_pk_add_f32 v[50:51], v[98:99], v[210:211] op_sel_hi:[1,0] neg_lo:[0,1] neg_hi:[0,1]
	v_pk_add_f32 v[58:59], v[106:107], v[210:211] op_sel_hi:[1,0] neg_lo:[0,1] neg_hi:[0,1]
	v_pk_add_f32 v[76:77], v[92:93], v[210:211] op_sel_hi:[1,0] neg_lo:[0,1] neg_hi:[0,1]
	v_pk_add_f32 v[60:61], v[108:109], v[210:211] op_sel_hi:[1,0] neg_lo:[0,1] neg_hi:[0,1]
	s_waitcnt lgkmcnt(0)
	v_readfirstlane_b32 s4, v17
	s_and_b32 s76, s4, 63
	s_sub_i32 s80, s94, s76
	v_pk_add_f32 v[78:79], v[94:95], v[210:211] op_sel_hi:[1,0] neg_lo:[0,1] neg_hi:[0,1]
	v_pk_add_f32 v[62:63], v[110:111], v[210:211] op_sel_hi:[1,0] neg_lo:[0,1] neg_hi:[0,1]
	v_pk_add_f32 v[80:81], v[96:97], v[210:211] op_sel_hi:[1,0] neg_lo:[0,1] neg_hi:[0,1]
	v_pk_add_f32 v[64:65], v[112:113], v[210:211] op_sel_hi:[1,0] neg_lo:[0,1] neg_hi:[0,1]
	s_cmp_gt_i32 s80, 2
	s_cbranch_scc0 .LBB0_1537
	s_cmp_lg_u32 s94, s76
	s_cbranch_scc0 .LBB0_1538

.LBB0_1551:
	v_add_u32_e32 v17, s90, v241
	ds_read_b64_tr_b16 v[8:9], v17 offset:24576
	ds_read_b64_tr_b16 v[10:11], v17 offset:25088
	s_waitcnt lgkmcnt(3)
	v_mfma_f32_32x32x16_bf16 v[82:97], v[174:177], v[126:129], 0
	v_add_f32_e32 v254, v66, v67
	v_add_f32_e32 v255, v68, v69
	v_cvt_pk_bf16_f32 v5, v66, v67
	v_add_f32_e32 v254, v70, v254
	v_cndmask_b32_e64 v142, 0, v5, s[92:93]
	v_cvt_pk_bf16_f32 v5, v68, v69
	v_add_f32_e32 v255, v71, v255
	v_cndmask_b32_e64 v143, 0, v5, s[92:93]
	ds_read_b64_tr_b16 v[12:13], v17 offset:28672
	ds_read_b64_tr_b16 v[14:15], v17 offset:29184
	s_waitcnt lgkmcnt(4)
	v_mfma_f32_32x32x16_bf16 v[98:113], v[166:169], v[126:129], 0
	v_add_f32_e32 v254, v72, v254
	v_add_f32_e32 v255, v73, v255
	v_add_f32_e32 v254, v74, v254
	v_add_f32_e32 v255, v75, v255
	v_cvt_pk_bf16_f32 v4, v70, v71
	v_cndmask_b32_e64 v144, 0, v4, s[92:93]
	v_cvt_pk_bf16_f32 v4, v72, v73
	v_cndmask_b32_e64 v145, 0, v4, s[92:93]
	ds_read_b64_tr_b16 v[4:5], v17 offset:25600
	ds_read_b64_tr_b16 v[6:7], v17 offset:26112
	s_waitcnt lgkmcnt(11)
	v_mfma_f32_32x32x16_bf16 v[82:97], v[170:173], v[122:125], v[82:97]
	v_add_f32_e32 v254, v76, v254
	v_add_f32_e32 v255, v77, v255
	v_cvt_pk_bf16_f32 v67, v74, v75
	v_add_f32_e32 v254, v78, v254
	v_cndmask_b32_e64 v138, 0, v67, s[92:93]
	v_cvt_pk_bf16_f32 v67, v76, v77
	v_add_f32_e32 v255, v79, v255
	v_cndmask_b32_e64 v139, 0, v67, s[92:93]
	ds_read_b64_tr_b16 v[178:179], v17 offset:29696
	ds_read_b64_tr_b16 v[180:181], v17 offset:30208
	s_waitcnt lgkmcnt(12)
	v_mfma_f32_32x32x16_bf16 v[98:113], v[162:165], v[122:125], v[98:113]
	v_add_f32_e32 v254, v80, v254
	v_add_f32_e32 v255, v81, v255
	v_cvt_pk_bf16_f32 v67, v78, v79
	v_add_f32_e32 v254, v50, v254
	v_cndmask_b32_e64 v140, 0, v67, s[92:93]
	v_cvt_pk_bf16_f32 v67, v80, v81
	v_add_f32_e32 v255, v51, v255
	v_cndmask_b32_e64 v141, 0, v67, s[92:93]
	ds_read_b64_tr_b16 v[182:183], v17 offset:26624
	ds_read_b64_tr_b16 v[184:185], v17 offset:27136
	s_waitcnt lgkmcnt(13)
	v_mfma_f32_32x32x16_bf16 v[82:97], v[158:161], v[118:121], v[82:97]
	v_add_f32_e32 v254, v52, v254
	v_add_f32_e32 v255, v53, v255
	v_cvt_pk_bf16_f32 v50, v50, v51
	v_add_f32_e32 v254, v54, v254
	v_cndmask_b32_e64 v134, 0, v50, s[92:93]
	v_cvt_pk_bf16_f32 v50, v52, v53
	v_add_f32_e32 v255, v55, v255
	v_cndmask_b32_e64 v135, 0, v50, s[92:93]
	ds_read_b64_tr_b16 v[186:187], v17 offset:30720
	ds_read_b64_tr_b16 v[188:189], v17 offset:31232
	s_waitcnt lgkmcnt(14)
	v_mfma_f32_32x32x16_bf16 v[98:113], v[154:157], v[118:121], v[98:113]
	v_add_f32_e32 v254, v56, v254
	v_add_f32_e32 v255, v57, v255
	v_cvt_pk_bf16_f32 v51, v54, v55
	v_add_f32_e32 v254, v58, v254
	v_cndmask_b32_e64 v136, 0, v51, s[92:93]
	v_cvt_pk_bf16_f32 v51, v56, v57
	v_add_f32_e32 v255, v59, v255
	v_cndmask_b32_e64 v137, 0, v51, s[92:93]
	ds_read_b64_tr_b16 v[190:191], v17 offset:27648
	ds_read_b64_tr_b16 v[192:193], v17 offset:28160
	s_waitcnt lgkmcnt(14)
	v_mfma_f32_32x32x16_bf16 v[82:97], v[150:153], v[114:117], v[82:97]
	v_add_f32_e32 v254, v60, v254
	v_add_f32_e32 v255, v61, v255
	v_cvt_pk_bf16_f32 v51, v58, v59
	v_add_f32_e32 v254, v62, v254
	v_cndmask_b32_e64 v130, 0, v51, s[92:93]
	v_cvt_pk_bf16_f32 v51, v60, v61
	v_add_f32_e32 v255, v63, v255
	v_cndmask_b32_e64 v131, 0, v51, s[92:93]
	ds_read_b64_tr_b16 v[194:195], v17 offset:31744
	ds_read_b64_tr_b16 v[196:197], v17 offset:32256
	v_mfma_f32_32x32x16_bf16 v[98:113], v[146:149], v[114:117], v[98:113]
	v_add_f32_e32 v254, v64, v254
	v_cvt_pk_bf16_f32 v50, v62, v63
	v_add_f32_e32 v255, v65, v255
	v_add_f32_e32 v17, v254, v255
	v_cndmask_b32_e64 v132, 0, v50, s[92:93]
	v_cvt_pk_bf16_f32 v50, v64, v65
	v_add_f32_e32 v17, 0, v17
	v_cndmask_b32_e64 v133, 0, v50, s[92:93]
	s_add_i32 s72, s85, 1
	s_cmp_ge_u32 s72, s82
	s_cselect_b64 s[80:81], -1, 0
	s_and_b64 vcc, exec, s[80:81]
	s_cbranch_vccnz .LBB0_1553
	v_mov_b32_e32 v50, s5
	ds_read_b32 v50, v50 offset:12
	s_waitcnt lgkmcnt(0)
	v_readfirstlane_b32 s72, v50
	s_lshl_b32 s72, s72, 13
	s_and_b32 s72, s72, 0x7e000
	s_add_u32 s72, s89, s72
	s_addc_u32 s73, s0, 0
	s_add_i32 s76, s84, s75
	s_mov_b32 s86, m0
	s_mov_b32 m0, s76
	s_nop 0
	global_load_lds_dwordx4 v238, s[72:73]
	s_mov_b32 m0, s86

.LBB0_1562:
	v_add_u32_e32 v14, s84, v241
	ds_read_b64_tr_b16 v[190:191], v14 offset:24576
	ds_read_b64_tr_b16 v[192:193], v14 offset:25088
	s_waitcnt lgkmcnt(9)
	v_mfma_f32_32x32x16_bf16 v[82:97], v[174:177], v[126:129], 0
	v_add_f32_e32 v254, v66, v67
	v_add_f32_e32 v255, v68, v69
	v_cvt_pk_bf16_f32 v5, v66, v67
	v_add_f32_e32 v254, v70, v254
	v_cndmask_b32_e64 v142, 0, v5, s[72:73]
	v_cvt_pk_bf16_f32 v5, v68, v69
	v_add_f32_e32 v255, v71, v255
	v_cndmask_b32_e64 v143, 0, v5, s[72:73]
	ds_read_b64_tr_b16 v[194:195], v14 offset:28672
	ds_read_b64_tr_b16 v[196:197], v14 offset:29184
	s_waitcnt lgkmcnt(10)
	v_mfma_f32_32x32x16_bf16 v[98:113], v[166:169], v[126:129], 0
	v_add_f32_e32 v254, v72, v254
	v_add_f32_e32 v255, v73, v255
	v_cvt_pk_bf16_f32 v5, v70, v71
	v_add_f32_e32 v254, v74, v254
	v_cndmask_b32_e64 v144, 0, v5, s[72:73]
	v_cvt_pk_bf16_f32 v5, v72, v73
	v_add_f32_e32 v255, v75, v255
	v_cndmask_b32_e64 v145, 0, v5, s[72:73]
	ds_read_b64_tr_b16 v[186:187], v14 offset:25600
	ds_read_b64_tr_b16 v[188:189], v14 offset:26112
	s_waitcnt lgkmcnt(11)
	v_mfma_f32_32x32x16_bf16 v[82:97], v[170:173], v[122:125], v[82:97]
	v_add_f32_e32 v254, v76, v254
	v_add_f32_e32 v255, v77, v255
	v_cvt_pk_bf16_f32 v5, v74, v75
	v_add_f32_e32 v254, v78, v254
	v_cndmask_b32_e64 v138, 0, v5, s[72:73]
	v_cvt_pk_bf16_f32 v5, v76, v77
	v_add_f32_e32 v255, v79, v255
	v_cndmask_b32_e64 v139, 0, v5, s[72:73]
	ds_read_b64_tr_b16 v[182:183], v14 offset:29696
	ds_read_b64_tr_b16 v[184:185], v14 offset:30208
	s_waitcnt lgkmcnt(12)
	v_mfma_f32_32x32x16_bf16 v[98:113], v[162:165], v[122:125], v[98:113]
	v_add_f32_e32 v254, v80, v254
	v_add_f32_e32 v255, v81, v255
	v_cvt_pk_bf16_f32 v5, v78, v79
	v_add_f32_e32 v254, v50, v254
	v_cndmask_b32_e64 v140, 0, v5, s[72:73]
	v_cvt_pk_bf16_f32 v5, v80, v81
	v_add_f32_e32 v255, v51, v255
	v_cndmask_b32_e64 v141, 0, v5, s[72:73]
	ds_read_b64_tr_b16 v[178:179], v14 offset:26624
	ds_read_b64_tr_b16 v[180:181], v14 offset:27136
	s_waitcnt lgkmcnt(13)
	v_mfma_f32_32x32x16_bf16 v[82:97], v[158:161], v[118:121], v[82:97]
	v_add_f32_e32 v254, v52, v254
	v_add_f32_e32 v255, v53, v255
	v_add_f32_e32 v254, v54, v254
	v_add_f32_e32 v255, v55, v255
	v_cvt_pk_bf16_f32 v4, v50, v51
	v_cndmask_b32_e64 v134, 0, v4, s[72:73]
	v_cvt_pk_bf16_f32 v4, v52, v53
	v_cndmask_b32_e64 v135, 0, v4, s[72:73]
	ds_read_b64_tr_b16 v[4:5], v14 offset:30720
	ds_read_b64_tr_b16 v[6:7], v14 offset:31232
	s_waitcnt lgkmcnt(14)
	v_mfma_f32_32x32x16_bf16 v[98:113], v[154:157], v[118:121], v[98:113]
	v_add_f32_e32 v254, v56, v254
	v_add_f32_e32 v255, v57, v255
	v_add_f32_e32 v254, v58, v254
	v_add_f32_e32 v255, v59, v255
	v_cvt_pk_bf16_f32 v8, v54, v55
	v_cndmask_b32_e64 v136, 0, v8, s[72:73]
	v_cvt_pk_bf16_f32 v8, v56, v57
	v_cndmask_b32_e64 v137, 0, v8, s[72:73]
	ds_read_b64_tr_b16 v[8:9], v14 offset:27648
	ds_read_b64_tr_b16 v[10:11], v14 offset:28160
	s_waitcnt lgkmcnt(14)
	v_mfma_f32_32x32x16_bf16 v[82:97], v[150:153], v[114:117], v[82:97]
	v_add_f32_e32 v254, v60, v254
	v_add_f32_e32 v255, v61, v255
	v_add_f32_e32 v254, v62, v254
	v_add_f32_e32 v255, v63, v255
	v_cvt_pk_bf16_f32 v12, v58, v59
	v_cndmask_b32_e64 v130, 0, v12, s[72:73]
	v_cvt_pk_bf16_f32 v12, v60, v61
	v_cndmask_b32_e64 v131, 0, v12, s[72:73]
	ds_read_b64_tr_b16 v[12:13], v14 offset:31744
	ds_read_b64_tr_b16 v[14:15], v14 offset:32256
	v_mfma_f32_32x32x16_bf16 v[98:113], v[146:149], v[114:117], v[98:113]
	v_add_f32_e32 v254, v64, v254
	v_add_f32_e32 v255, v65, v255
	v_add_f32_e32 v50, v254, v255
	v_add_f32_e32 v242, 0, v50
	v_cvt_pk_bf16_f32 v50, v62, v63
	v_cndmask_b32_e64 v132, 0, v50, s[72:73]
	v_cvt_pk_bf16_f32 v50, v64, v65
	v_cndmask_b32_e64 v133, 0, v50, s[72:73]
	s_add_i32 s76, s85, 2
	s_cmp_ge_u32 s76, s82
	s_cselect_b64 s[90:91], -1, 0
	s_and_b64 vcc, exec, s[90:91]
	s_cbranch_vccnz .LBB0_1564
	v_mov_b32_e32 v50, s5
	ds_read_b32 v50, v50 offset:16
	s_waitcnt lgkmcnt(0)
	v_readfirstlane_b32 s84, v50
	s_lshl_b32 s84, s84, 13
	s_and_b32 s84, s84, 0x7e000
	s_add_u32 s86, s89, s84
	s_addc_u32 s87, s0, 0
	s_add_i32 s84, s4, s75
	s_mov_b32 s92, m0
	s_mov_b32 m0, s84
	s_nop 0
	global_load_lds_dwordx4 v238, s[86:87]
	s_mov_b32 m0, s92

.LBB0_1608:
	v_readlane_b32 s14, v252, 19
	v_readlane_b32 s12, v252, 36
	v_readlane_b32 s18, v252, 38
	v_readlane_b32 s15, v252, 20
	v_readlane_b32 s16, v252, 32
	v_readlane_b32 s63, v252, 35
	v_readlane_b32 s13, v252, 37
	v_readlane_b32 s19, v252, 39
	v_add_u32_e32 v2, s4, v241
	ds_read_b64_tr_b16 v[4:5], v2 offset:24576
	ds_read_b64_tr_b16 v[6:7], v2 offset:25088
	v_add_f32_e32 v254, v66, v67
	v_add_f32_e32 v255, v68, v69
	v_cvt_pk_bf16_f32 v9, v66, v67
	v_add_f32_e32 v254, v70, v254
	v_cndmask_b32_e64 v142, 0, v9, s[92:93]
	v_cvt_pk_bf16_f32 v9, v68, v69
	v_add_f32_e32 v255, v71, v255
	v_cndmask_b32_e64 v143, 0, v9, s[92:93]
	s_waitcnt lgkmcnt(3)
	v_mfma_f32_32x32x16_bf16 v[82:97], v[174:177], v[126:129], 0
	ds_read_b64_tr_b16 v[12:13], v2 offset:28672
	ds_read_b64_tr_b16 v[14:15], v2 offset:29184
	v_add_f32_e32 v254, v72, v254
	v_add_f32_e32 v255, v73, v255
	v_add_f32_e32 v254, v74, v254
	v_add_f32_e32 v255, v75, v255
	v_cvt_pk_bf16_f32 v8, v70, v71
	v_cndmask_b32_e64 v144, 0, v8, s[92:93]
	v_cvt_pk_bf16_f32 v8, v72, v73
	v_cndmask_b32_e64 v145, 0, v8, s[92:93]
	s_waitcnt lgkmcnt(4)
	v_mfma_f32_32x32x16_bf16 v[98:113], v[166:169], v[126:129], 0
	ds_read_b64_tr_b16 v[8:9], v2 offset:25600
	ds_read_b64_tr_b16 v[10:11], v2 offset:26112
	v_add_f32_e32 v254, v76, v254
	v_add_f32_e32 v255, v77, v255
	v_cvt_pk_bf16_f32 v17, v74, v75
	v_add_f32_e32 v254, v78, v254
	v_cndmask_b32_e64 v138, 0, v17, s[92:93]
	v_cvt_pk_bf16_f32 v17, v76, v77
	v_add_f32_e32 v255, v79, v255
	v_cndmask_b32_e64 v139, 0, v17, s[92:93]
	v_mfma_f32_32x32x16_bf16 v[82:97], v[170:173], v[122:125], v[82:97]
	ds_read_b64_tr_b16 v[126:127], v2 offset:29696
	ds_read_b64_tr_b16 v[128:129], v2 offset:30208
	v_add_f32_e32 v254, v80, v254
	v_add_f32_e32 v255, v81, v255
	v_cvt_pk_bf16_f32 v17, v78, v79
	v_add_f32_e32 v254, v50, v254
	v_cndmask_b32_e64 v140, 0, v17, s[92:93]
	v_cvt_pk_bf16_f32 v17, v80, v81
	v_add_f32_e32 v255, v51, v255
	v_cndmask_b32_e64 v141, 0, v17, s[92:93]
	v_mfma_f32_32x32x16_bf16 v[98:113], v[162:165], v[122:125], v[98:113]
	ds_read_b64_tr_b16 v[122:123], v2 offset:26624
	ds_read_b64_tr_b16 v[124:125], v2 offset:27136
	v_add_f32_e32 v254, v52, v254
	v_add_f32_e32 v255, v53, v255
	v_cvt_pk_bf16_f32 v17, v50, v51
	v_add_f32_e32 v254, v54, v254
	v_cndmask_b32_e64 v134, 0, v17, s[92:93]
	v_cvt_pk_bf16_f32 v17, v52, v53
	v_add_f32_e32 v255, v55, v255
	v_cndmask_b32_e64 v135, 0, v17, s[92:93]
	v_mfma_f32_32x32x16_bf16 v[82:97], v[158:161], v[118:121], v[82:97]
	ds_read_b64_tr_b16 v[158:159], v2 offset:30720
	ds_read_b64_tr_b16 v[160:161], v2 offset:31232
	v_add_f32_e32 v254, v56, v254
	v_add_f32_e32 v255, v57, v255
	v_cvt_pk_bf16_f32 v17, v54, v55
	v_add_f32_e32 v254, v58, v254
	v_cndmask_b32_e64 v136, 0, v17, s[92:93]
	v_cvt_pk_bf16_f32 v17, v56, v57
	v_add_f32_e32 v255, v59, v255
	v_cndmask_b32_e64 v137, 0, v17, s[92:93]
	v_mfma_f32_32x32x16_bf16 v[98:113], v[154:157], v[118:121], v[98:113]
	ds_read_b64_tr_b16 v[118:119], v2 offset:27648
	ds_read_b64_tr_b16 v[120:121], v2 offset:28160
	v_add_f32_e32 v254, v60, v254
	v_add_f32_e32 v255, v61, v255
	v_cvt_pk_bf16_f32 v17, v58, v59
	v_add_f32_e32 v254, v62, v254
	v_cndmask_b32_e64 v130, 0, v17, s[92:93]
	v_cvt_pk_bf16_f32 v17, v60, v61
	v_add_f32_e32 v255, v63, v255
	v_cndmask_b32_e64 v131, 0, v17, s[92:93]
	v_mfma_f32_32x32x16_bf16 v[82:97], v[150:153], v[114:117], v[82:97]
	ds_read_b64_tr_b16 v[150:151], v2 offset:31744
	ds_read_b64_tr_b16 v[152:153], v2 offset:32256
	v_add_f32_e32 v254, v64, v254
	v_cvt_pk_bf16_f32 v16, v62, v63
	v_add_f32_e32 v255, v65, v255
	v_add_f32_e32 v2, v254, v255
	v_cndmask_b32_e64 v132, 0, v16, s[92:93]
	v_cvt_pk_bf16_f32 v16, v64, v65
	v_add_f32_e32 v2, 0, v2
	v_cndmask_b32_e64 v133, 0, v16, s[92:93]
	v_mfma_f32_32x32x16_bf16 v[98:113], v[146:149], v[114:117], v[98:113]
	s_lshl_b32 s4, s82, 2
	s_add_i32 s4, s4, 0
	s_add_i32 s4, s4, 0x1dabc
	v_mov_b32_e32 v16, s4
	ds_read_b32 v16, v16
	v_pk_add_f32 v[66:67], v[82:83], v[210:211] op_sel_hi:[1,0] neg_lo:[0,1] neg_hi:[0,1]
	s_nop 5
	v_pk_add_f32 v[50:51], v[98:99], v[210:211] op_sel_hi:[1,0] neg_lo:[0,1] neg_hi:[0,1]
	v_pk_add_f32 v[68:69], v[84:85], v[210:211] op_sel_hi:[1,0] neg_lo:[0,1] neg_hi:[0,1]
	v_pk_add_f32 v[52:53], v[100:101], v[210:211] op_sel_hi:[1,0] neg_lo:[0,1] neg_hi:[0,1]
	s_waitcnt lgkmcnt(0)
	v_readfirstlane_b32 s4, v16
	s_and_b32 s6, s4, 63
	s_sub_i32 s5, s94, s6
	v_pk_add_f32 v[70:71], v[86:87], v[210:211] op_sel_hi:[1,0] neg_lo:[0,1] neg_hi:[0,1]
	v_pk_add_f32 v[54:55], v[102:103], v[210:211] op_sel_hi:[1,0] neg_lo:[0,1] neg_hi:[0,1]
	v_pk_add_f32 v[72:73], v[88:89], v[210:211] op_sel_hi:[1,0] neg_lo:[0,1] neg_hi:[0,1]
	v_pk_add_f32 v[56:57], v[104:105], v[210:211] op_sel_hi:[1,0] neg_lo:[0,1] neg_hi:[0,1]
	v_pk_add_f32 v[74:75], v[90:91], v[210:211] op_sel_hi:[1,0] neg_lo:[0,1] neg_hi:[0,1]
	v_pk_add_f32 v[58:59], v[106:107], v[210:211] op_sel_hi:[1,0] neg_lo:[0,1] neg_hi:[0,1]
	v_pk_add_f32 v[76:77], v[92:93], v[210:211] op_sel_hi:[1,0] neg_lo:[0,1] neg_hi:[0,1]
	v_pk_add_f32 v[60:61], v[108:109], v[210:211] op_sel_hi:[1,0] neg_lo:[0,1] neg_hi:[0,1]
	v_pk_add_f32 v[78:79], v[94:95], v[210:211] op_sel_hi:[1,0] neg_lo:[0,1] neg_hi:[0,1]
	v_pk_add_f32 v[62:63], v[110:111], v[210:211] op_sel_hi:[1,0] neg_lo:[0,1] neg_hi:[0,1]
	v_pk_add_f32 v[80:81], v[96:97], v[210:211] op_sel_hi:[1,0] neg_lo:[0,1] neg_hi:[0,1]
	v_pk_add_f32 v[64:65], v[112:113], v[210:211] op_sel_hi:[1,0] neg_lo:[0,1] neg_hi:[0,1]
	s_cmp_gt_i32 s5, 2
	s_cbranch_scc1 .LBB0_1610
	s_lshl_b32 s7, s5, 8
	v_sub_u32_e32 v16, v236, v235
	s_add_i32 s7, s7, s33
	v_lshl_add_u32 v111, v16, 2, s7
	ds_read_b32 v16, v111 offset:256
	ds_read_b32 v82, v111 offset:128
	ds_read_b32 v17, v111 offset:252
	ds_read_b32 v83, v111 offset:124
	ds_read_b32 v84, v111 offset:248
	ds_read_b32 v86, v111 offset:120
	ds_read_b32 v85, v111 offset:244
	ds_read_b32 v87, v111 offset:116
	ds_read_b32 v88, v111 offset:224
	ds_read_b32 v90, v111 offset:96
	ds_read_b32 v89, v111 offset:220
	ds_read_b32 v91, v111 offset:92
	ds_read_b32 v92, v111 offset:216
	ds_read_b32 v94, v111 offset:88
	ds_read_b32 v93, v111 offset:212
	ds_read_b32 v95, v111 offset:84
	ds_read_b32 v96, v111 offset:192
	ds_read_b32 v98, v111 offset:64
	ds_read_b32 v97, v111 offset:188
	ds_read_b32 v99, v111 offset:60
	ds_read_b32 v100, v111 offset:184
	ds_read_b32 v102, v111 offset:56
	ds_read_b32 v101, v111 offset:180
	ds_read_b32 v103, v111 offset:52
	ds_read_b32 v104, v111 offset:160
	ds_read_b32 v106, v111 offset:32
	ds_read_b32 v105, v111 offset:156
	ds_read_b32 v107, v111 offset:28
	ds_read_b32 v108, v111 offset:152
	ds_read_b32 v110, v111 offset:24
	ds_read_b32 v109, v111 offset:148
	ds_read_b32 v111, v111 offset:20
	s_waitcnt lgkmcnt(14)
	v_pk_add_f32 v[66:67], v[66:67], v[16:17]
	v_pk_add_f32 v[68:69], v[68:69], v[84:85]
	v_pk_add_f32 v[70:71], v[70:71], v[88:89]
	v_pk_add_f32 v[72:73], v[72:73], v[92:93]
	s_waitcnt lgkmcnt(13)
	v_pk_add_f32 v[74:75], v[74:75], v[96:97]
	s_waitcnt lgkmcnt(9)
	v_pk_add_f32 v[76:77], v[76:77], v[100:101]
	s_waitcnt lgkmcnt(5)
	v_pk_add_f32 v[78:79], v[78:79], v[104:105]
	s_waitcnt lgkmcnt(1)
	v_pk_add_f32 v[80:81], v[80:81], v[108:109]
	v_pk_add_f32 v[50:51], v[50:51], v[82:83]
	v_pk_add_f32 v[52:53], v[52:53], v[86:87]
	v_pk_add_f32 v[54:55], v[54:55], v[90:91]
	v_pk_add_f32 v[56:57], v[56:57], v[94:95]
	v_pk_add_f32 v[58:59], v[58:59], v[98:99]
	v_pk_add_f32 v[60:61], v[60:61], v[102:103]
	v_pk_add_f32 v[62:63], v[62:63], v[106:107]
	s_waitcnt lgkmcnt(0)
	v_pk_add_f32 v[64:65], v[64:65], v[110:111]

; #define SBAR() __builtin_amdgcn_sched_barrier(0)
;   #define PKW(P,B) cvtpk_s(P[B],P[B+1])
;   #define PKW(P,B) cvtpk_s(P[B],P[B+1])
; template<bool WIN,int THRL> __device__ __forceinline__ void nsa_branch_pipe(const bf16*__restrict__ Kb,const bf16*__restrict__ Vb,const __attribute__((address_space(3))) int*tl,int NT,int qc,const bf16x8*qr,unsigned selbits, ...
;     ...
;   { float sacc=pB0[0]+pB0[1]; _Pragma("unroll") for(int r=2;r<16;++r)sacc+=pB0[r]; _Pragma("unroll") for(int r=0;r<16;++r)sacc+=pB1[r]; l_reg+=(amB?sacc:0.f);
;     pw0=(u32x4){PKW(pB0,0)&amB,PKW(pB0,2)&amB,PKW(pB0,4)&amB,PKW(pB0,6)&amB};pw1=(u32x4){PKW(pB0,8)&amB,PKW(pB0,10)&amB,PKW(pB0,12)&amB,PKW(pB0,14)&amB};pw2=(u32x4){PKW(pB1,0)&amB,PKW(pB1,2)&amB,PKW(pB1,4)&amB,PKW(pB1,6)&amB};pw3=(u32x4){PKW(pB1,8)&amB,PKW(pB1,10)&amB,PKW(pB1,12)&amB,PKW(pB1,14)&amB};
;     SBAR(); pv(o,vb0+sl_cur,PAF(0),PAF(1),PAF(2),PAF(3)); }
;     ...
;   {auto rr=__builtin_amdgcn_permlane32_swap(__float_as_uint(l_reg),__float_as_uint(l_reg),false,false);l_out=__uint_as_float(rr[0])+__uint_as_float(rr[1]);}
; __device__ __forceinline__ void nsa_unit(int b, int g, int qc, const bf16* Q, const bf16* KV, const bf16* KC2, size_t kvstride, size_t kc2stride, const float* gates, const float* lutg, bf16* O, char* shm) {
;     ...
;       nsa_branch_pipe<true, 32>(kvb + 4 * kvstride, kvb + 5 * kvstride, (const __attribute__((address_space(3))) int*)(shm3 + L_TL) + 48, NTw, qc, qr, 0xffffffffu, luth, shm, lt, ob);
;       const float gw = gl[128 + lane]; stash_acc(stash, ob, lt > 0.f ? gw * __builtin_amdgcn_rcpf(lt) : 0.f, wsf, lane, r32, hi, false); }
.LBB0_1618:
	v_add_f32_e32 v254, v66, v67
	v_add_f32_e32 v255, v68, v69
	v_add_f32_e32 v254, v70, v254
	v_add_f32_e32 v255, v71, v255
	v_add_f32_e32 v254, v72, v254
	v_add_f32_e32 v255, v73, v255
	v_add_f32_e32 v254, v74, v254
	v_add_f32_e32 v255, v75, v255
	v_add_f32_e32 v254, v76, v254
	v_add_f32_e32 v255, v77, v255
	v_add_f32_e32 v254, v78, v254
	v_add_f32_e32 v255, v79, v255
	v_add_f32_e32 v254, v80, v254
	v_add_f32_e32 v255, v81, v255
	v_add_f32_e32 v254, v50, v254
	v_add_f32_e32 v255, v51, v255
	v_add_f32_e32 v254, v52, v254
	v_add_f32_e32 v255, v53, v255
	v_add_f32_e32 v254, v54, v254
	v_add_f32_e32 v255, v55, v255
	v_add_f32_e32 v254, v56, v254
	v_add_f32_e32 v255, v57, v255
	v_add_f32_e32 v254, v58, v254
	v_add_f32_e32 v255, v59, v255
	v_add_f32_e32 v254, v60, v254
	v_add_f32_e32 v255, v61, v255
	v_add_f32_e32 v254, v62, v254
	v_add_f32_e32 v255, v63, v255
	v_add_f32_e32 v254, v64, v254
	v_add_f32_e32 v255, v65, v255
	v_add_f32_e32 v4, v254, v255
	v_cvt_pk_bf16_f32 v17, v58, v59
	s_cmp_lg_u32 0, -1
	v_cndmask_b32_e64 v4, 0, v4, s[4:5]
	v_cvt_pk_bf16_f32 v12, v50, v51
	v_cndmask_b32_e64 v50, 0, v17, s[4:5]
	v_cvt_pk_bf16_f32 v17, v60, v61
	s_cselect_b32 s6, 0, 0
	v_add_f32_e32 v2, v2, v4
	v_cvt_pk_bf16_f32 v4, v66, v67
	v_cndmask_b32_e64 v51, 0, v17, s[4:5]
	v_cvt_pk_bf16_f32 v17, v62, v63
	s_addk_i32 s6, 0x6000
	v_cndmask_b32_e64 v4, 0, v4, s[4:5]
	v_cvt_pk_bf16_f32 v5, v68, v69
	v_cvt_pk_bf16_f32 v6, v70, v71
	v_cvt_pk_bf16_f32 v7, v72, v73
	v_cvt_pk_bf16_f32 v8, v74, v75
	v_cvt_pk_bf16_f32 v9, v76, v77
	v_cvt_pk_bf16_f32 v10, v78, v79
	v_cvt_pk_bf16_f32 v11, v80, v81
	v_cvt_pk_bf16_f32 v13, v52, v53
	v_cvt_pk_bf16_f32 v14, v54, v55
	v_cvt_pk_bf16_f32 v15, v56, v57
	v_cndmask_b32_e64 v52, 0, v17, s[4:5]
	v_cvt_pk_bf16_f32 v17, v64, v65
	v_add3_u32 v16, v234, s6, v230
	v_cndmask_b32_e64 v5, 0, v5, s[4:5]
	v_cndmask_b32_e64 v6, 0, v6, s[4:5]
	v_cndmask_b32_e64 v7, 0, v7, s[4:5]
	v_cndmask_b32_e64 v8, 0, v8, s[4:5]
	v_cndmask_b32_e64 v9, 0, v9, s[4:5]
	v_cndmask_b32_e64 v10, 0, v10, s[4:5]
	v_cndmask_b32_e64 v11, 0, v11, s[4:5]
	v_cndmask_b32_e64 v12, 0, v12, s[4:5]
	v_cndmask_b32_e64 v13, 0, v13, s[4:5]
	v_cndmask_b32_e64 v14, 0, v14, s[4:5]
	v_cndmask_b32_e64 v15, 0, v15, s[4:5]
	v_cndmask_b32_e64 v53, 0, v17, s[4:5]
	v_add3_u32 v16, v16, v233, s84
	ds_read_b64_tr_b16 v[54:55],v16 offset:0
	ds_read_b64_tr_b16 v[56:57],v16 offset:512
	ds_read_b64_tr_b16 v[58:59],v16 offset:1024
	ds_read_b64_tr_b16 v[60:61],v16 offset:1536
	ds_read_b64_tr_b16 v[62:63],v16 offset:2048
	ds_read_b64_tr_b16 v[64:65],v16 offset:2560
	ds_read_b64_tr_b16 v[66:67],v16 offset:3072
	ds_read_b64_tr_b16 v[68:69],v16 offset:3584
	s_waitcnt lgkmcnt(0)
	s_nop 0
	v_mfma_f32_32x32x16_bf16 v[34:49], v[4:7], v[54:57], v[34:49]
	ds_read_b64_tr_b16 v[54:55],v16 offset:4096
	ds_read_b64_tr_b16 v[56:57],v16 offset:4608
	v_mfma_f32_32x32x16_bf16 v[34:49], v[8:11], v[58:61], v[34:49]
	ds_read_b64_tr_b16 v[58:59],v16 offset:5120
	ds_read_b64_tr_b16 v[60:61],v16 offset:5632
	v_mfma_f32_32x32x16_bf16 v[34:49], v[12:15], v[62:65], v[34:49]
	ds_read_b64_tr_b16 v[62:63],v16 offset:6144
	ds_read_b64_tr_b16 v[64:65],v16 offset:6656
	v_mfma_f32_32x32x16_bf16 v[34:49], v[50:53], v[66:69], v[34:49]
	ds_read_b64_tr_b16 v[66:67],v16 offset:7168
	ds_read_b64_tr_b16 v[68:69],v16 offset:7680
	s_waitcnt lgkmcnt(0)
	v_mfma_f32_32x32x16_bf16 v[18:33], v[4:7], v[54:57], v[18:33]
	s_waitcnt lgkmcnt(0)
	s_barrier
	v_mov_b32_e32 v4, v2
	s_nop 1
	v_permlane32_swap_b32_e32 v2, v4
	v_mfma_f32_32x32x16_bf16 v[18:33], v[8:11], v[58:61], v[18:33]
	v_mfma_f32_32x32x16_bf16 v[18:33], v[12:15], v[62:65], v[18:33]
	v_mfma_f32_32x32x16_bf16 v[18:33], v[50:53], v[66:69], v[18:33]
	s_and_saveexec_b64 s[4:5], s[2:3]
	s_cbranch_execz .LBB0_1368
	v_add_f32_e32 v2, v2, v4
	ds_read_b32 v4, v227 offset:512
	v_rcp_f32_e32 v5, v2
	v_cmp_lt_f32_e32 vcc, 0, v2
	v_lshl_add_u32 v6, v212, 2, s20
	s_waitcnt lgkmcnt(0)
	v_mul_f32_e32 v4, v5, v4
	v_cndmask_b32_e32 v2, 0, v4, vcc
	ds_write_b32 v6, v2 offset:49152
	s_branch .LBB0_1368
